# m23 + P-phase WUP/BAL staging by LDS-DMA + barrier leader relay without waiting for its TOPGEN add + one s_nop 15 (16 wait states, 12 needed) at the six epilogue entries
# baseline (speedup 1.0000x reference)
; #define PG8_BAR __builtin_amdgcn_s_barrier()
; template <class Epi, class Sched, bool F8 = false>
; DI void gemm_phase(LAS unsigned char* lds, const int K, const Sched& S, const Epi& E) {
;     ...
;         if (wr == 0) PG8_BAR;
;         if constexpr (F8) asm volatile("s_nop 15\n\ts_nop 15" ::: "memory");
;         E(acc, cur, wr, wc, fr, fq);
.LBB0_279:
	s_nop 15
	s_add_i32 s4, s62, -5
	v_mov_b32_e32 v6, v1
	v_mov_b32_e32 v18, v5
	s_cmp_gt_u32 s4, 2
	s_mov_b64 s[30:31], -1
	v_mov_b32_e32 v248, v203
	v_mov_b64_e32 v[250:251], v[228:229]
	s_cbranch_scc0 .LBB0_281
	s_sub_i32 s4, s62, 35
	s_sub_i32 s5, s62, 30
	s_cmp_lt_u32 s4, 3
	s_cselect_b32 s43, s5, s62
	s_mov_b64 s[30:31], 0

; #define GAS __attribute__((address_space(1)))
;     DI void operator()(const f32x4 (&acc)[2][2][4][2], const Unit& u, int wr, int wc, int fr, int fq) const {
;     ...
;         const int row0 = u.pm * 256 + wr * 64 + fr, col0 = u.pn * 256 + wc * 32 + 8 * fq; constexpr float k = W8_INV / 255.0f;
;         u32x2 g[2][4][2];
; #pragma unroll
;         for (int ai = 0; ai < 2; ++ai)
; #pragma unroll
;             for (int m = 0; m < 4; ++m)
; #pragma unroll
;                 for (int bj = 0; bj < 2; ++bj) g[ai][m][bj] = *(const GAS u32x2*)(gt + (size_t)(row0 + ai * 128 + m * 16) * 2048 + col0 + bj * 128);
; #pragma unroll
;         for (int ai = 0; ai < 2; ++ai) {
;             u32x2 ov[4][2];
;             if (ADD) {
; #pragma unroll
;                 for (int m = 0; m < 4; ++m)
; #pragma unroll
;                     for (int bj = 0; bj < 2; ++bj) ov[m][bj] = *(const GAS u32x2*)((const GAS unsigned char*)mix + (size_t)(row0 + ai * 128 + m * 16) * 1024 + col0 + bj * 128);
;             }
;             asm volatile("" ::: "memory");
; #pragma unroll
;             for (int m = 0; m < 4; ++m) { const size_t r = (size_t)(row0 + ai * 128 + m * 16); u32x2 o8v[2];
; #pragma unroll
;                 for (int bj = 0; bj < 2; ++bj) {
;                     const u32x2 gg = g[ai][m][bj];
;                     f32x4 v0 = acc[ai][bj][m][0], v1 = acc[ai][bj][m][1];
;                     v0[0] *= (float)((gg.x >> 0) & 0xffu) * k; v0[1] *= (float)((gg.x >> 8) & 0xffu) * k; v0[2] *= (float)((gg.x >> 16) & 0xffu) * k; v0[3] *= (float)((gg.x >> 24) & 0xffu) * k;
;                     v1[0] *= (float)((gg.y >> 0) & 0xffu) * k; v1[1] *= (float)((gg.y >> 8) & 0xffu) * k; v1[2] *= (float)((gg.y >> 16) & 0xffu) * k; v1[3] *= (float)((gg.y >> 24) & 0xffu) * k;
;                     if (ADD) { const u32x2 o = ov[m][bj]; const f32x2 oa = __builtin_amdgcn_cvt_pk_f32_fp8((int)o.x, false), ob = __builtin_amdgcn_cvt_pk_f32_fp8((int)o.x, true), oc = __builtin_amdgcn_cvt_pk_f32_fp8((int)o.y, false), od = __builtin_amdgcn_cvt_pk_f32_fp8((int)o.y, true);
;                         v0[0] += oa[0]; v0[1] += oa[1]; v0[2] += ob[0]; v0[3] += ob[1]; v1[0] += oc[0]; v1[1] += oc[1]; v1[2] += od[0]; v1[3] += od[1];
;                     }
;                     o8v[bj].x = pk4_fp8(v0[0], v0[1], v0[2], v0[3]); o8v[bj].y = pk4_fp8(v1[0], v1[1], v1[2], v1[3]); }
.LBB0_906:
	s_lshl_b32 s6, s54, 8
	v_mov_b32_e32 v198, v5
	v_mov_b32_e32 v6, v1
	s_add_i32 s6, s6, s83
	s_nop 15
	s_andn2_b64 vcc, exec, s[40:41]
	v_add_u32_e32 v212, s6, v6
	s_lshl_b32 s6, s55, 8
	s_or_b32 s6, s6, s84
	v_lshl_add_u32 v10, v198, 3, s6
	v_ashrrev_i32_e32 v11, 31, v10
	v_ashrrev_i32_e32 v213, 31, v212
	v_lshl_add_u64 v[12:13], s[42:43], 0, v[10:11]
	v_lshlrev_b64 v[6:7], 11, v[212:213]
	v_lshl_add_u64 v[8:9], v[12:13], 0, v[6:7]
	global_load_dwordx2 v[6:7], v[8:9], off
	s_nop 0
	global_load_dwordx2 v[8:9], v[8:9], off offset:128
	v_add_u32_e32 v192, 16, v212
	v_ashrrev_i32_e32 v193, 31, v192
	v_lshlrev_b64 v[14:15], 11, v[192:193]
	v_lshl_add_u64 v[14:15], v[12:13], 0, v[14:15]
	global_load_dwordx2 v[196:197], v[14:15], off
	global_load_dwordx2 v[194:195], v[14:15], off offset:128
	v_add_u32_e32 v186, 32, v212
	v_ashrrev_i32_e32 v187, 31, v186
	v_lshlrev_b64 v[14:15], 11, v[186:187]
	v_add_u32_e32 v180, 48, v212
	v_lshl_add_u64 v[14:15], v[12:13], 0, v[14:15]
	v_ashrrev_i32_e32 v181, 31, v180
	global_load_dwordx2 v[190:191], v[14:15], off
	global_load_dwordx2 v[188:189], v[14:15], off offset:128
	v_lshlrev_b64 v[14:15], 11, v[180:181]
	v_add_u32_e32 v32, 0x80, v212
	v_lshl_add_u64 v[14:15], v[12:13], 0, v[14:15]
	v_ashrrev_i32_e32 v33, 31, v32
	global_load_dwordx2 v[184:185], v[14:15], off
	global_load_dwordx2 v[182:183], v[14:15], off offset:128
	v_lshlrev_b64 v[14:15], 11, v[32:33]
	v_add_u32_e32 v26, 0x90, v212
	v_lshl_add_u64 v[14:15], v[12:13], 0, v[14:15]
	v_ashrrev_i32_e32 v27, 31, v26
	global_load_dwordx2 v[36:37], v[14:15], off
	global_load_dwordx2 v[34:35], v[14:15], off offset:128
	v_lshlrev_b64 v[14:15], 11, v[26:27]
	v_add_u32_e32 v20, 0xa0, v212
	v_lshl_add_u64 v[14:15], v[12:13], 0, v[14:15]
	v_ashrrev_i32_e32 v21, 31, v20
	global_load_dwordx2 v[30:31], v[14:15], off
	global_load_dwordx2 v[28:29], v[14:15], off offset:128
	v_lshlrev_b64 v[14:15], 11, v[20:21]
	v_lshl_add_u64 v[14:15], v[12:13], 0, v[14:15]
	global_load_dwordx2 v[24:25], v[14:15], off
	global_load_dwordx2 v[22:23], v[14:15], off offset:128
	v_add_u32_e32 v14, 0xb0, v212
	v_ashrrev_i32_e32 v15, 31, v14
	v_lshlrev_b64 v[16:17], 11, v[14:15]
	v_lshl_add_u64 v[12:13], v[12:13], 0, v[16:17]
	global_load_dwordx2 v[18:19], v[12:13], off
	global_load_dwordx2 v[16:17], v[12:13], off offset:128
	v_bfe_i32 v12, v198, 0, 1
	v_and_b32_e32 v12, 0x78, v12
	v_mov_b32_e32 v13, v4
	v_lshlrev_b64 v[32:33], 10, v[32:33]
	v_lshl_add_u64 v[32:33], s[30:31], 0, v[32:33]
	v_lshl_add_u64 v[32:33], v[32:33], 0, v[10:11]
	v_lshl_add_u64 v[32:33], v[32:33], 0, v[12:13]
	v_lshlrev_b64 v[26:27], 10, v[26:27]
	v_lshl_add_u64 v[26:27], s[30:31], 0, v[26:27]
	v_lshl_add_u64 v[26:27], v[26:27], 0, v[10:11]
	v_lshl_add_u64 v[26:27], v[26:27], 0, v[12:13]
	v_lshlrev_b64 v[20:21], 10, v[20:21]
	v_lshl_add_u64 v[20:21], s[30:31], 0, v[20:21]
	v_lshl_add_u64 v[20:21], v[20:21], 0, v[10:11]
	v_lshl_add_u64 v[20:21], v[20:21], 0, v[12:13]
	v_lshlrev_b64 v[14:15], 10, v[14:15]
	v_lshl_add_u64 v[14:15], s[30:31], 0, v[14:15]
	s_mov_b64 s[54:55], -1
	s_waitcnt vmcnt(0)
	v_cvt_f32_ubyte0_e32 v198, v6
	v_mul_f32_e32 v198, 0x38808081, v198
	v_mul_f32_e32 v162, v162, v198
	v_cvt_f32_ubyte1_e32 v198, v6
	v_mul_f32_e32 v198, 0x38808081, v198
	v_mul_f32_e32 v163, v163, v198
	v_cvt_f32_ubyte2_e32 v198, v6
	v_cvt_f32_ubyte3_e32 v6, v6
	v_mul_f32_e32 v6, 0x38808081, v6
	v_mul_f32_e32 v165, v165, v6
	v_cvt_f32_ubyte0_e32 v6, v7
	v_mul_f32_e32 v6, 0x38808081, v6
	v_mul_f32_e32 v158, v158, v6
	v_cvt_f32_ubyte1_e32 v6, v7
	v_mul_f32_e32 v6, 0x38808081, v6
	v_mul_f32_e32 v159, v159, v6
	v_cvt_f32_ubyte2_e32 v6, v7
	v_mul_f32_e32 v6, 0x38808081, v6
	v_mul_f32_e32 v160, v160, v6
	v_cvt_f32_ubyte3_e32 v6, v7
	v_mul_f32_e32 v6, 0x38808081, v6
	v_mul_f32_e32 v161, v161, v6
	v_med3_f32 v7, v162, s35, v225
	v_med3_f32 v162, v163, s35, v225
	v_mov_b32_e32 v6, v4
	v_cvt_pk_fp8_f32 v6, v7, v162
	v_mul_f32_e32 v198, 0x38808081, v198
	v_mul_f32_e32 v164, v164, v198
	v_med3_f32 v7, v164, s35, v225
	v_med3_f32 v162, v165, s35, v225
	v_cvt_pk_fp8_f32 v6, v7, v162 op_sel:[0,0,1]
	v_med3_f32 v158, v158, s35, v225
	v_med3_f32 v159, v159, s35, v225
	v_mov_b32_e32 v7, v4
	v_cvt_pk_fp8_f32 v7, v158, v159
	v_med3_f32 v158, v160, s35, v225
	v_med3_f32 v159, v161, s35, v225
	v_cvt_pk_fp8_f32 v7, v158, v159 op_sel:[0,0,1]
	v_cvt_f32_ubyte0_e32 v158, v8
	v_mul_f32_e32 v158, 0x38808081, v158
	v_mul_f32_e32 v154, v154, v158
	v_cvt_f32_ubyte1_e32 v158, v8
	v_mul_f32_e32 v158, 0x38808081, v158
	v_mul_f32_e32 v155, v155, v158
	v_cvt_f32_ubyte2_e32 v158, v8
	v_cvt_f32_ubyte3_e32 v8, v8
	v_mul_f32_e32 v8, 0x38808081, v8
	v_mul_f32_e32 v157, v157, v8
	v_cvt_f32_ubyte0_e32 v8, v9
	v_mul_f32_e32 v8, 0x38808081, v8
	v_mul_f32_e32 v150, v150, v8
	v_cvt_f32_ubyte1_e32 v8, v9
	v_mul_f32_e32 v8, 0x38808081, v8
	v_mul_f32_e32 v151, v151, v8
	v_cvt_f32_ubyte2_e32 v8, v9
	v_mul_f32_e32 v8, 0x38808081, v8
	v_mul_f32_e32 v152, v152, v8
	v_cvt_f32_ubyte3_e32 v8, v9
	v_mul_f32_e32 v8, 0x38808081, v8
	v_mul_f32_e32 v153, v153, v8
	v_med3_f32 v9, v154, s35, v225
	v_med3_f32 v154, v155, s35, v225
	v_mov_b32_e32 v8, v4
	v_cvt_pk_fp8_f32 v8, v9, v154
	v_mul_f32_e32 v158, 0x38808081, v158
	v_mul_f32_e32 v156, v156, v158
	v_med3_f32 v9, v156, s35, v225
	v_med3_f32 v154, v157, s35, v225
	v_cvt_pk_fp8_f32 v8, v9, v154 op_sel:[0,0,1]
	v_med3_f32 v150, v150, s35, v225
	v_med3_f32 v151, v151, s35, v225
	v_mov_b32_e32 v9, v4
	v_cvt_pk_fp8_f32 v9, v150, v151
	v_med3_f32 v150, v152, s35, v225
	v_med3_f32 v151, v153, s35, v225
	v_permlane16_swap_b32_e32 v6, v8
	v_cvt_pk_fp8_f32 v9, v150, v151 op_sel:[0,0,1]
	v_lshlrev_b64 v[150:151], 10, v[212:213]
; DI unsigned pk4_fp8(float a, float b, float c_, float d) { int w = 0; w = __builtin_amdgcn_cvt_pk_fp8_f32(clamp8(a), clamp8(b), w, false); w = __builtin_amdgcn_cvt_pk_fp8_f32(clamp8(c_), clamp8(d), w, true); return (unsigned)w; }
;     DI void operator()(const f32x4 (&acc)[2][2][4][2], const Unit& u, int wr, int wc, int fr, int fq) const {
;     ...
;             for (int m = 0; m < 4; ++m) { const size_t r = (size_t)(row0 + ai * 128 + m * 16); u32x2 o8v[2];
; #pragma unroll
;                 for (int bj = 0; bj < 2; ++bj) {
;                     const u32x2 gg = g[ai][m][bj];
;                     f32x4 v0 = acc[ai][bj][m][0], v1 = acc[ai][bj][m][1];
;                     v0[0] *= (float)((gg.x >> 0) & 0xffu) * k; v0[1] *= (float)((gg.x >> 8) & 0xffu) * k; v0[2] *= (float)((gg.x >> 16) & 0xffu) * k; v0[3] *= (float)((gg.x >> 24) & 0xffu) * k;
;                     v1[0] *= (float)((gg.y >> 0) & 0xffu) * k; v1[1] *= (float)((gg.y >> 8) & 0xffu) * k; v1[2] *= (float)((gg.y >> 16) & 0xffu) * k; v1[3] *= (float)((gg.y >> 24) & 0xffu) * k;
;                     if (ADD) { const u32x2 o = ov[m][bj]; const f32x2 oa = __builtin_amdgcn_cvt_pk_f32_fp8((int)o.x, false), ob = __builtin_amdgcn_cvt_pk_f32_fp8((int)o.x, true), oc = __builtin_amdgcn_cvt_pk_f32_fp8((int)o.y, false), od = __builtin_amdgcn_cvt_pk_f32_fp8((int)o.y, true);
;                         v0[0] += oa[0]; v0[1] += oa[1]; v0[2] += ob[0]; v0[3] += ob[1]; v1[0] += oc[0]; v1[1] += oc[1]; v1[2] += od[0]; v1[3] += od[1];
;                     }
;                     o8v[bj].x = pk4_fp8(v0[0], v0[1], v0[2], v0[3]); o8v[bj].y = pk4_fp8(v1[0], v1[1], v1[2], v1[3]); }
;                 st_pair16((ADD ? mix8 : (unsigned char*)mix) + r * 1024 + col0, 128, o8v[0], o8v[1], fq); }
	v_lshl_add_u64 v[150:151], s[30:31], 0, v[150:151]
	v_lshl_add_u64 v[150:151], v[150:151], 0, v[10:11]
	v_permlane16_swap_b32_e32 v7, v9
	v_lshl_add_u64 v[150:151], v[150:151], 0, v[12:13]
	global_store_dwordx4 v[150:151], v[6:9], off
	s_nop 1
	v_cvt_f32_ubyte0_e32 v6, v196
	v_mul_f32_e32 v6, 0x38808081, v6
	v_mul_f32_e32 v6, v146, v6
	v_cvt_f32_ubyte0_e32 v146, v197
	v_mul_f32_e32 v146, 0x38808081, v146
	v_mul_f32_e32 v142, v142, v146
	v_cvt_f32_ubyte1_e32 v146, v197
	v_mul_f32_e32 v146, 0x38808081, v146
	v_mul_f32_e32 v143, v143, v146
	v_cvt_f32_ubyte2_e32 v146, v197
	v_cvt_f32_ubyte1_e32 v7, v196
	v_mul_f32_e32 v146, 0x38808081, v146
	v_mul_f32_e32 v7, 0x38808081, v7
	v_mul_f32_e32 v144, v144, v146
	v_cvt_f32_ubyte3_e32 v146, v197
	v_mul_f32_e32 v7, v147, v7
	v_mul_f32_e32 v146, 0x38808081, v146
	v_mul_f32_e32 v145, v145, v146
	v_med3_f32 v146, v6, s35, v225
	v_med3_f32 v7, v7, s35, v225
	v_mov_b32_e32 v6, v4
	v_cvt_f32_ubyte2_e32 v8, v196
	v_cvt_f32_ubyte3_e32 v9, v196
	v_cvt_pk_fp8_f32 v6, v146, v7
	v_mul_f32_e32 v8, 0x38808081, v8
	v_mul_f32_e32 v9, 0x38808081, v9
	v_mul_f32_e32 v8, v148, v8
	v_mul_f32_e32 v9, v149, v9
	v_med3_f32 v7, v8, s35, v225
	v_med3_f32 v8, v9, s35, v225
	v_cvt_pk_fp8_f32 v6, v7, v8 op_sel:[0,0,1]
	v_med3_f32 v8, v142, s35, v225
	v_med3_f32 v9, v143, s35, v225
	v_mov_b32_e32 v7, v4
	v_cvt_pk_fp8_f32 v7, v8, v9
	v_med3_f32 v8, v144, s35, v225
	v_med3_f32 v9, v145, s35, v225
	v_cvt_pk_fp8_f32 v7, v8, v9 op_sel:[0,0,1]
	v_cvt_f32_ubyte0_e32 v8, v194
	v_mul_f32_e32 v8, 0x38808081, v8
	v_mul_f32_e32 v8, v138, v8
	v_cvt_f32_ubyte2_e32 v138, v194
	v_mul_f32_e32 v138, 0x38808081, v138
	v_mul_f32_e32 v138, v140, v138
	v_cvt_f32_ubyte0_e32 v140, v195
	v_mul_f32_e32 v140, 0x38808081, v140
	v_mul_f32_e32 v134, v134, v140
	v_cvt_f32_ubyte1_e32 v140, v195
	v_mul_f32_e32 v140, 0x38808081, v140
	v_mul_f32_e32 v135, v135, v140
	v_cvt_f32_ubyte2_e32 v140, v195
	v_cvt_f32_ubyte1_e32 v9, v194
	v_mul_f32_e32 v140, 0x38808081, v140
	v_mul_f32_e32 v9, 0x38808081, v9
	v_mul_f32_e32 v136, v136, v140
	v_cvt_f32_ubyte3_e32 v140, v195
	v_mul_f32_e32 v9, v139, v9
	v_mul_f32_e32 v140, 0x38808081, v140
	v_mul_f32_e32 v137, v137, v140
	v_med3_f32 v140, v8, s35, v225
	v_med3_f32 v9, v9, s35, v225
	v_mov_b32_e32 v8, v4
	v_cvt_f32_ubyte3_e32 v139, v194
	v_cvt_pk_fp8_f32 v8, v140, v9
	v_mul_f32_e32 v139, 0x38808081, v139
	v_mul_f32_e32 v139, v141, v139
	v_med3_f32 v9, v138, s35, v225
	v_med3_f32 v138, v139, s35, v225
	v_cvt_pk_fp8_f32 v8, v9, v138 op_sel:[0,0,1]
	v_med3_f32 v134, v134, s35, v225
	v_med3_f32 v135, v135, s35, v225
	v_mov_b32_e32 v9, v4
	v_cvt_pk_fp8_f32 v9, v134, v135
	v_med3_f32 v134, v136, s35, v225
	v_med3_f32 v135, v137, s35, v225
	v_permlane16_swap_b32_e32 v6, v8
	v_cvt_pk_fp8_f32 v9, v134, v135 op_sel:[0,0,1]
	v_lshlrev_b64 v[134:135], 10, v[192:193]
	v_lshl_add_u64 v[134:135], s[30:31], 0, v[134:135]
	v_lshl_add_u64 v[134:135], v[134:135], 0, v[10:11]
	v_permlane16_swap_b32_e32 v7, v9
	v_lshl_add_u64 v[134:135], v[134:135], 0, v[12:13]
	global_store_dwordx4 v[134:135], v[6:9], off
	s_nop 1
	v_cvt_f32_ubyte0_e32 v6, v190
	v_mul_f32_e32 v6, 0x38808081, v6
	v_mul_f32_e32 v6, v130, v6
	v_cvt_f32_ubyte0_e32 v130, v191
	v_mul_f32_e32 v130, 0x38808081, v130
	v_mul_f32_e32 v126, v126, v130
	v_cvt_f32_ubyte1_e32 v130, v191
	v_mul_f32_e32 v130, 0x38808081, v130
	v_mul_f32_e32 v127, v127, v130
	v_cvt_f32_ubyte2_e32 v130, v191
	v_cvt_f32_ubyte1_e32 v7, v190
	v_mul_f32_e32 v130, 0x38808081, v130
	v_mul_f32_e32 v7, 0x38808081, v7
	v_mul_f32_e32 v128, v128, v130
	v_cvt_f32_ubyte3_e32 v130, v191
	v_mul_f32_e32 v7, v131, v7
	v_mul_f32_e32 v130, 0x38808081, v130
	v_mul_f32_e32 v129, v129, v130
	v_med3_f32 v130, v6, s35, v225
	v_med3_f32 v7, v7, s35, v225
	v_mov_b32_e32 v6, v4
	v_cvt_f32_ubyte2_e32 v8, v190
	v_cvt_f32_ubyte3_e32 v9, v190
	v_cvt_pk_fp8_f32 v6, v130, v7
	v_mul_f32_e32 v8, 0x38808081, v8
	v_mul_f32_e32 v9, 0x38808081, v9
	v_mul_f32_e32 v8, v132, v8
	v_mul_f32_e32 v9, v133, v9
	v_med3_f32 v7, v8, s35, v225
	v_med3_f32 v8, v9, s35, v225
	v_cvt_pk_fp8_f32 v6, v7, v8 op_sel:[0,0,1]
	v_med3_f32 v8, v126, s35, v225
	v_med3_f32 v9, v127, s35, v225
	v_mov_b32_e32 v7, v4
	v_cvt_pk_fp8_f32 v7, v8, v9
	v_med3_f32 v8, v128, s35, v225
	v_med3_f32 v9, v129, s35, v225
	v_cvt_pk_fp8_f32 v7, v8, v9 op_sel:[0,0,1]
	v_cvt_f32_ubyte0_e32 v8, v188
	v_mul_f32_e32 v8, 0x38808081, v8
	v_mul_f32_e32 v8, v122, v8
	v_cvt_f32_ubyte2_e32 v122, v188
	v_mul_f32_e32 v122, 0x38808081, v122
	v_mul_f32_e32 v122, v124, v122
	v_cvt_f32_ubyte0_e32 v124, v189
	v_mul_f32_e32 v124, 0x38808081, v124
	v_mul_f32_e32 v118, v118, v124
	v_cvt_f32_ubyte1_e32 v124, v189
	v_mul_f32_e32 v124, 0x38808081, v124
	v_mul_f32_e32 v119, v119, v124
	v_cvt_f32_ubyte2_e32 v124, v189
	v_cvt_f32_ubyte1_e32 v9, v188
	v_mul_f32_e32 v124, 0x38808081, v124
	v_mul_f32_e32 v9, 0x38808081, v9
	v_mul_f32_e32 v120, v120, v124
	v_cvt_f32_ubyte3_e32 v124, v189
	v_mul_f32_e32 v9, v123, v9
	v_mul_f32_e32 v124, 0x38808081, v124
	v_mul_f32_e32 v121, v121, v124
	v_med3_f32 v124, v8, s35, v225
	v_med3_f32 v9, v9, s35, v225
	v_mov_b32_e32 v8, v4
	v_cvt_f32_ubyte3_e32 v123, v188
	v_cvt_pk_fp8_f32 v8, v124, v9
	v_mul_f32_e32 v123, 0x38808081, v123
	v_mul_f32_e32 v123, v125, v123
	v_med3_f32 v9, v122, s35, v225
	v_med3_f32 v122, v123, s35, v225
	v_cvt_pk_fp8_f32 v8, v9, v122 op_sel:[0,0,1]
	v_med3_f32 v118, v118, s35, v225
	v_med3_f32 v119, v119, s35, v225
	v_mov_b32_e32 v9, v4
	v_cvt_pk_fp8_f32 v9, v118, v119
	v_med3_f32 v118, v120, s35, v225
	v_med3_f32 v119, v121, s35, v225
	v_permlane16_swap_b32_e32 v6, v8
	v_cvt_pk_fp8_f32 v9, v118, v119 op_sel:[0,0,1]
	v_lshlrev_b64 v[118:119], 10, v[186:187]
; DI unsigned pk4_fp8(float a, float b, float c_, float d) { int w = 0; w = __builtin_amdgcn_cvt_pk_fp8_f32(clamp8(a), clamp8(b), w, false); w = __builtin_amdgcn_cvt_pk_fp8_f32(clamp8(c_), clamp8(d), w, true); return (unsigned)w; }
;     DI void operator()(const f32x4 (&acc)[2][2][4][2], const Unit& u, int wr, int wc, int fr, int fq) const {
;     ...
;             for (int m = 0; m < 4; ++m) { const size_t r = (size_t)(row0 + ai * 128 + m * 16); u32x2 o8v[2];
; #pragma unroll
;                 for (int bj = 0; bj < 2; ++bj) {
;                     const u32x2 gg = g[ai][m][bj];
;                     f32x4 v0 = acc[ai][bj][m][0], v1 = acc[ai][bj][m][1];
;                     v0[0] *= (float)((gg.x >> 0) & 0xffu) * k; v0[1] *= (float)((gg.x >> 8) & 0xffu) * k; v0[2] *= (float)((gg.x >> 16) & 0xffu) * k; v0[3] *= (float)((gg.x >> 24) & 0xffu) * k;
;                     v1[0] *= (float)((gg.y >> 0) & 0xffu) * k; v1[1] *= (float)((gg.y >> 8) & 0xffu) * k; v1[2] *= (float)((gg.y >> 16) & 0xffu) * k; v1[3] *= (float)((gg.y >> 24) & 0xffu) * k;
;                     if (ADD) { const u32x2 o = ov[m][bj]; const f32x2 oa = __builtin_amdgcn_cvt_pk_f32_fp8((int)o.x, false), ob = __builtin_amdgcn_cvt_pk_f32_fp8((int)o.x, true), oc = __builtin_amdgcn_cvt_pk_f32_fp8((int)o.y, false), od = __builtin_amdgcn_cvt_pk_f32_fp8((int)o.y, true);
;                         v0[0] += oa[0]; v0[1] += oa[1]; v0[2] += ob[0]; v0[3] += ob[1]; v1[0] += oc[0]; v1[1] += oc[1]; v1[2] += od[0]; v1[3] += od[1];
;                     }
;                     o8v[bj].x = pk4_fp8(v0[0], v0[1], v0[2], v0[3]); o8v[bj].y = pk4_fp8(v1[0], v1[1], v1[2], v1[3]); }
;                 st_pair16((ADD ? mix8 : (unsigned char*)mix) + r * 1024 + col0, 128, o8v[0], o8v[1], fq); }
	v_lshl_add_u64 v[118:119], s[30:31], 0, v[118:119]
	v_lshl_add_u64 v[118:119], v[118:119], 0, v[10:11]
	v_permlane16_swap_b32_e32 v7, v9
	v_lshl_add_u64 v[118:119], v[118:119], 0, v[12:13]
	global_store_dwordx4 v[118:119], v[6:9], off
	s_nop 1
	v_cvt_f32_ubyte0_e32 v6, v184
	v_mul_f32_e32 v6, 0x38808081, v6
	v_mul_f32_e32 v6, v114, v6
	v_cvt_f32_ubyte0_e32 v114, v185
	v_mul_f32_e32 v114, 0x38808081, v114
	v_mul_f32_e32 v110, v110, v114
	v_cvt_f32_ubyte1_e32 v114, v185
	v_mul_f32_e32 v114, 0x38808081, v114
	v_mul_f32_e32 v111, v111, v114
	v_cvt_f32_ubyte2_e32 v114, v185
	v_cvt_f32_ubyte1_e32 v7, v184
	v_mul_f32_e32 v114, 0x38808081, v114
	v_mul_f32_e32 v7, 0x38808081, v7
	v_mul_f32_e32 v112, v112, v114
	v_cvt_f32_ubyte3_e32 v114, v185
	v_mul_f32_e32 v7, v115, v7
	v_mul_f32_e32 v114, 0x38808081, v114
	v_mul_f32_e32 v113, v113, v114
	v_med3_f32 v114, v6, s35, v225
	v_med3_f32 v7, v7, s35, v225
	v_mov_b32_e32 v6, v4
	v_cvt_f32_ubyte2_e32 v8, v184
	v_cvt_f32_ubyte3_e32 v9, v184
	v_cvt_pk_fp8_f32 v6, v114, v7
	v_mul_f32_e32 v8, 0x38808081, v8
	v_mul_f32_e32 v9, 0x38808081, v9
	v_mul_f32_e32 v8, v116, v8
	v_mul_f32_e32 v9, v117, v9
	v_med3_f32 v7, v8, s35, v225
	v_med3_f32 v8, v9, s35, v225
	v_cvt_pk_fp8_f32 v6, v7, v8 op_sel:[0,0,1]
	v_med3_f32 v8, v110, s35, v225
	v_med3_f32 v9, v111, s35, v225
	v_mov_b32_e32 v7, v4
	v_cvt_pk_fp8_f32 v7, v8, v9
	v_med3_f32 v8, v112, s35, v225
	v_med3_f32 v9, v113, s35, v225
	v_cvt_pk_fp8_f32 v7, v8, v9 op_sel:[0,0,1]
	v_cvt_f32_ubyte0_e32 v8, v182
	v_mul_f32_e32 v8, 0x38808081, v8
	v_mul_f32_e32 v8, v98, v8
	v_cvt_f32_ubyte2_e32 v98, v182
	v_mul_f32_e32 v98, 0x38808081, v98
	v_mul_f32_e32 v98, v100, v98
	v_cvt_f32_ubyte0_e32 v100, v183
	v_mul_f32_e32 v100, 0x38808081, v100
	v_mul_f32_e32 v94, v94, v100
	v_cvt_f32_ubyte1_e32 v100, v183
	v_mul_f32_e32 v100, 0x38808081, v100
	v_mul_f32_e32 v95, v95, v100
	v_cvt_f32_ubyte2_e32 v100, v183
	v_cvt_f32_ubyte1_e32 v9, v182
	v_mul_f32_e32 v100, 0x38808081, v100
	v_mul_f32_e32 v9, 0x38808081, v9
	v_mul_f32_e32 v96, v96, v100
	v_cvt_f32_ubyte3_e32 v100, v183
	v_mul_f32_e32 v9, v99, v9
	v_mul_f32_e32 v100, 0x38808081, v100
	v_mul_f32_e32 v97, v97, v100
	v_med3_f32 v100, v8, s35, v225
	v_med3_f32 v9, v9, s35, v225
	v_mov_b32_e32 v8, v4
	v_cvt_f32_ubyte3_e32 v99, v182
	v_cvt_pk_fp8_f32 v8, v100, v9
	v_mul_f32_e32 v99, 0x38808081, v99
	v_mul_f32_e32 v99, v101, v99
	v_med3_f32 v9, v98, s35, v225
	v_med3_f32 v98, v99, s35, v225
	v_cvt_pk_fp8_f32 v8, v9, v98 op_sel:[0,0,1]
	v_med3_f32 v94, v94, s35, v225
	v_med3_f32 v95, v95, s35, v225
	v_mov_b32_e32 v9, v4
	v_cvt_pk_fp8_f32 v9, v94, v95
	v_med3_f32 v94, v96, s35, v225
	v_med3_f32 v95, v97, s35, v225
	v_permlane16_swap_b32_e32 v6, v8
	v_cvt_pk_fp8_f32 v9, v94, v95 op_sel:[0,0,1]
	v_lshlrev_b64 v[94:95], 10, v[180:181]
	v_lshl_add_u64 v[94:95], s[30:31], 0, v[94:95]
	v_lshl_add_u64 v[94:95], v[94:95], 0, v[10:11]
	v_permlane16_swap_b32_e32 v7, v9
	v_lshl_add_u64 v[94:95], v[94:95], 0, v[12:13]
	global_store_dwordx4 v[94:95], v[6:9], off
	v_cvt_f32_ubyte1_e32 v94, v37
	v_mul_f32_e32 v94, 0x38808081, v94
	v_cvt_f32_ubyte0_e32 v6, v36
	v_cvt_f32_ubyte1_e32 v7, v36
	v_mul_f32_e32 v6, 0x38808081, v6
	v_mul_f32_e32 v7, 0x38808081, v7
	v_mul_f32_e32 v6, v106, v6
	v_mul_f32_e32 v7, v107, v7
	v_med3_f32 v96, v6, s35, v225
	v_med3_f32 v7, v7, s35, v225
	v_mov_b32_e32 v6, v4
	v_cvt_f32_ubyte2_e32 v8, v36
	v_cvt_f32_ubyte3_e32 v9, v36
	v_cvt_pk_fp8_f32 v6, v96, v7
	v_mul_f32_e32 v8, 0x38808081, v8
	v_mul_f32_e32 v9, 0x38808081, v9
	v_cvt_f32_ubyte0_e32 v36, v37
	v_mul_f32_e32 v8, v108, v8
	v_mul_f32_e32 v9, v109, v9
	v_mul_f32_e32 v36, 0x38808081, v36
	v_mul_f32_e32 v36, v102, v36
	v_mul_f32_e32 v94, v103, v94
	v_cvt_f32_ubyte2_e32 v95, v37
	v_cvt_f32_ubyte3_e32 v37, v37
	v_med3_f32 v7, v8, s35, v225
	v_med3_f32 v8, v9, s35, v225
	v_mul_f32_e32 v37, 0x38808081, v37
	v_cvt_pk_fp8_f32 v6, v7, v8 op_sel:[0,0,1]
	v_med3_f32 v8, v36, s35, v225
	v_med3_f32 v9, v94, s35, v225
	v_mov_b32_e32 v7, v4
	v_mul_f32_e32 v37, v105, v37
	v_cvt_pk_fp8_f32 v7, v8, v9
	v_mul_f32_e32 v95, 0x38808081, v95
	v_med3_f32 v9, v37, s35, v225
	v_cvt_f32_ubyte0_e32 v37, v35
	v_mul_f32_e32 v95, v104, v95
	v_mul_f32_e32 v37, 0x38808081, v37
	v_med3_f32 v8, v95, s35, v225
	v_mul_f32_e32 v37, v86, v37
	v_cvt_f32_ubyte1_e32 v86, v35
	v_cvt_pk_fp8_f32 v7, v8, v9 op_sel:[0,0,1]
	v_cvt_f32_ubyte0_e32 v8, v34
	v_cvt_f32_ubyte1_e32 v9, v34
	v_mul_f32_e32 v86, 0x38808081, v86
	v_mul_f32_e32 v8, 0x38808081, v8
	v_mul_f32_e32 v9, 0x38808081, v9
	v_mul_f32_e32 v86, v87, v86
	v_cvt_f32_ubyte2_e32 v87, v35
	v_mul_f32_e32 v8, v90, v8
	v_mul_f32_e32 v9, v91, v9
	v_mul_f32_e32 v87, 0x38808081, v87
	v_mul_f32_e32 v87, v88, v87
	v_med3_f32 v88, v8, s35, v225
	v_med3_f32 v9, v9, s35, v225
	v_mov_b32_e32 v8, v4
	v_cvt_f32_ubyte2_e32 v36, v34
	v_cvt_f32_ubyte3_e32 v34, v34
	v_cvt_pk_fp8_f32 v8, v88, v9
	v_mul_f32_e32 v36, 0x38808081, v36
	v_mul_f32_e32 v34, 0x38808081, v34
	v_mul_f32_e32 v36, v92, v36
	v_mul_f32_e32 v34, v93, v34
	v_med3_f32 v9, v36, s35, v225
	v_med3_f32 v34, v34, s35, v225
	v_cvt_pk_fp8_f32 v8, v9, v34 op_sel:[0,0,1]
	v_med3_f32 v34, v37, s35, v225
	v_med3_f32 v36, v86, s35, v225
	v_mov_b32_e32 v9, v4
	v_cvt_f32_ubyte3_e32 v35, v35
	v_cvt_pk_fp8_f32 v9, v34, v36
	v_mul_f32_e32 v35, 0x38808081, v35
	v_mul_f32_e32 v35, v89, v35
	v_med3_f32 v34, v87, s35, v225
	v_med3_f32 v35, v35, s35, v225
	v_cvt_pk_fp8_f32 v9, v34, v35 op_sel:[0,0,1]
	v_permlane16_swap_b32_e32 v6, v8
	s_nop 0
	v_permlane16_swap_b32_e32 v7, v9
	global_store_dwordx4 v[32:33], v[6:9], off
	v_cvt_f32_ubyte1_e32 v32, v31
	v_mul_f32_e32 v32, 0x38808081, v32
	v_cvt_f32_ubyte0_e32 v6, v30
	v_cvt_f32_ubyte1_e32 v7, v30
; DI unsigned pk4_fp8(float a, float b, float c_, float d) { int w = 0; w = __builtin_amdgcn_cvt_pk_fp8_f32(clamp8(a), clamp8(b), w, false); w = __builtin_amdgcn_cvt_pk_fp8_f32(clamp8(c_), clamp8(d), w, true); return (unsigned)w; }
;     DI void operator()(const f32x4 (&acc)[2][2][4][2], const Unit& u, int wr, int wc, int fr, int fq) const {
;     ...
;             for (int m = 0; m < 4; ++m) { const size_t r = (size_t)(row0 + ai * 128 + m * 16); u32x2 o8v[2];
; #pragma unroll
;                 for (int bj = 0; bj < 2; ++bj) {
;                     const u32x2 gg = g[ai][m][bj];
;                     f32x4 v0 = acc[ai][bj][m][0], v1 = acc[ai][bj][m][1];
;                     v0[0] *= (float)((gg.x >> 0) & 0xffu) * k; v0[1] *= (float)((gg.x >> 8) & 0xffu) * k; v0[2] *= (float)((gg.x >> 16) & 0xffu) * k; v0[3] *= (float)((gg.x >> 24) & 0xffu) * k;
;                     v1[0] *= (float)((gg.y >> 0) & 0xffu) * k; v1[1] *= (float)((gg.y >> 8) & 0xffu) * k; v1[2] *= (float)((gg.y >> 16) & 0xffu) * k; v1[3] *= (float)((gg.y >> 24) & 0xffu) * k;
;                     if (ADD) { const u32x2 o = ov[m][bj]; const f32x2 oa = __builtin_amdgcn_cvt_pk_f32_fp8((int)o.x, false), ob = __builtin_amdgcn_cvt_pk_f32_fp8((int)o.x, true), oc = __builtin_amdgcn_cvt_pk_f32_fp8((int)o.y, false), od = __builtin_amdgcn_cvt_pk_f32_fp8((int)o.y, true);
;                         v0[0] += oa[0]; v0[1] += oa[1]; v0[2] += ob[0]; v0[3] += ob[1]; v1[0] += oc[0]; v1[1] += oc[1]; v1[2] += od[0]; v1[3] += od[1];
;                     }
;                     o8v[bj].x = pk4_fp8(v0[0], v0[1], v0[2], v0[3]); o8v[bj].y = pk4_fp8(v1[0], v1[1], v1[2], v1[3]); }
;                 st_pair16((ADD ? mix8 : (unsigned char*)mix) + r * 1024 + col0, 128, o8v[0], o8v[1], fq); }
	v_mul_f32_e32 v6, 0x38808081, v6
	v_mul_f32_e32 v7, 0x38808081, v7
	v_mul_f32_e32 v6, v82, v6
	v_mul_f32_e32 v7, v83, v7
	v_med3_f32 v34, v6, s35, v225
	v_med3_f32 v7, v7, s35, v225
	v_mov_b32_e32 v6, v4
	v_cvt_f32_ubyte2_e32 v8, v30
	v_cvt_f32_ubyte3_e32 v9, v30
	v_cvt_pk_fp8_f32 v6, v34, v7
	v_mul_f32_e32 v8, 0x38808081, v8
	v_mul_f32_e32 v9, 0x38808081, v9
	v_cvt_f32_ubyte0_e32 v30, v31
	v_mul_f32_e32 v8, v84, v8
	v_mul_f32_e32 v9, v85, v9
	v_mul_f32_e32 v30, 0x38808081, v30
	v_mul_f32_e32 v30, v78, v30
	v_mul_f32_e32 v32, v79, v32
	v_med3_f32 v7, v8, s35, v225
	v_med3_f32 v8, v9, s35, v225
	v_cvt_pk_fp8_f32 v6, v7, v8 op_sel:[0,0,1]
	v_med3_f32 v8, v30, s35, v225
	v_med3_f32 v9, v32, s35, v225
	v_mov_b32_e32 v7, v4
	v_cvt_f32_ubyte2_e32 v33, v31
	v_cvt_f32_ubyte3_e32 v31, v31
	v_cvt_pk_fp8_f32 v7, v8, v9
	v_mul_f32_e32 v33, 0x38808081, v33
	v_mul_f32_e32 v31, 0x38808081, v31
	v_mul_f32_e32 v33, v80, v33
	v_mul_f32_e32 v31, v81, v31
	v_med3_f32 v8, v33, s35, v225
	v_med3_f32 v9, v31, s35, v225
	v_cvt_pk_fp8_f32 v7, v8, v9 op_sel:[0,0,1]
	v_cvt_f32_ubyte0_e32 v8, v28
	v_cvt_f32_ubyte1_e32 v9, v28
	v_mul_f32_e32 v8, 0x38808081, v8
	v_mul_f32_e32 v9, 0x38808081, v9
	v_mul_f32_e32 v8, v74, v8
	v_mul_f32_e32 v9, v75, v9
	v_med3_f32 v34, v8, s35, v225
	v_med3_f32 v9, v9, s35, v225
	v_mov_b32_e32 v8, v4
	v_cvt_f32_ubyte2_e32 v30, v28
	v_cvt_f32_ubyte3_e32 v28, v28
	v_cvt_pk_fp8_f32 v8, v34, v9
	v_mul_f32_e32 v30, 0x38808081, v30
	v_mul_f32_e32 v28, 0x38808081, v28
	v_cvt_f32_ubyte0_e32 v31, v29
	v_cvt_f32_ubyte1_e32 v32, v29
	v_mul_f32_e32 v30, v76, v30
	v_mul_f32_e32 v28, v77, v28
	v_mul_f32_e32 v31, 0x38808081, v31
	v_mul_f32_e32 v32, 0x38808081, v32
	v_mul_f32_e32 v31, v70, v31
	v_mul_f32_e32 v32, v71, v32
	v_med3_f32 v9, v30, s35, v225
	v_med3_f32 v28, v28, s35, v225
	v_cvt_pk_fp8_f32 v8, v9, v28 op_sel:[0,0,1]
	v_med3_f32 v28, v31, s35, v225
	v_med3_f32 v30, v32, s35, v225
	v_mov_b32_e32 v9, v4
	v_cvt_f32_ubyte2_e32 v33, v29
	v_cvt_f32_ubyte3_e32 v29, v29
	v_cvt_pk_fp8_f32 v9, v28, v30
	v_mul_f32_e32 v33, 0x38808081, v33
	v_mul_f32_e32 v29, 0x38808081, v29
	v_mul_f32_e32 v33, v72, v33
	v_mul_f32_e32 v29, v73, v29
	v_med3_f32 v28, v33, s35, v225
	v_med3_f32 v29, v29, s35, v225
	v_cvt_pk_fp8_f32 v9, v28, v29 op_sel:[0,0,1]
	v_permlane16_swap_b32_e32 v6, v8
	v_lshl_add_u64 v[10:11], v[14:15], 0, v[10:11]
	v_permlane16_swap_b32_e32 v7, v9
	global_store_dwordx4 v[26:27], v[6:9], off
	v_cvt_f32_ubyte1_e32 v26, v25
	v_mul_f32_e32 v26, 0x38808081, v26
	v_cvt_f32_ubyte0_e32 v6, v24
	v_cvt_f32_ubyte1_e32 v7, v24
	v_mul_f32_e32 v6, 0x38808081, v6
	v_mul_f32_e32 v7, 0x38808081, v7
	v_mul_f32_e32 v6, v66, v6
	v_mul_f32_e32 v7, v67, v7
	v_med3_f32 v28, v6, s35, v225
	v_med3_f32 v7, v7, s35, v225
	v_mov_b32_e32 v6, v4
	v_cvt_f32_ubyte2_e32 v8, v24
	v_cvt_f32_ubyte3_e32 v9, v24
	v_cvt_pk_fp8_f32 v6, v28, v7
	v_mul_f32_e32 v8, 0x38808081, v8
	v_mul_f32_e32 v9, 0x38808081, v9
	v_cvt_f32_ubyte0_e32 v24, v25
	v_mul_f32_e32 v8, v68, v8
	v_mul_f32_e32 v9, v69, v9
	v_mul_f32_e32 v24, 0x38808081, v24
	v_mul_f32_e32 v24, v62, v24
	v_mul_f32_e32 v26, v63, v26
	v_med3_f32 v7, v8, s35, v225
	v_med3_f32 v8, v9, s35, v225
	v_cvt_pk_fp8_f32 v6, v7, v8 op_sel:[0,0,1]
	v_med3_f32 v8, v24, s35, v225
	v_med3_f32 v9, v26, s35, v225
	v_mov_b32_e32 v7, v4
	v_cvt_f32_ubyte2_e32 v27, v25
	v_cvt_f32_ubyte3_e32 v25, v25
	v_cvt_pk_fp8_f32 v7, v8, v9
	v_mul_f32_e32 v27, 0x38808081, v27
	v_mul_f32_e32 v25, 0x38808081, v25
	v_mul_f32_e32 v27, v64, v27
	v_mul_f32_e32 v25, v65, v25
	v_med3_f32 v8, v27, s35, v225
	v_med3_f32 v9, v25, s35, v225
	v_cvt_pk_fp8_f32 v7, v8, v9 op_sel:[0,0,1]
	v_cvt_f32_ubyte0_e32 v8, v22
	v_cvt_f32_ubyte1_e32 v9, v22
	v_mul_f32_e32 v8, 0x38808081, v8
	v_mul_f32_e32 v9, 0x38808081, v9
	v_mul_f32_e32 v8, v58, v8
	v_mul_f32_e32 v9, v59, v9
; DI unsigned pk4_fp8(float a, float b, float c_, float d) { int w = 0; w = __builtin_amdgcn_cvt_pk_fp8_f32(clamp8(a), clamp8(b), w, false); w = __builtin_amdgcn_cvt_pk_fp8_f32(clamp8(c_), clamp8(d), w, true); return (unsigned)w; }
; #define PG8_BAR __builtin_amdgcn_s_barrier()
; template <class Epi, class Sched, bool F8 = false>
; DI void gemm_phase(LAS unsigned char* lds, const int K, const Sched& S, const Epi& E) {
;     ...
;         if (!has_next) break;
;         if constexpr (!F8)
; #pragma unroll
;         for (int a = 0; a < 2; ++a)
; #pragma unroll
;             for (int b = 0; b < 2; ++b)
; #pragma unroll
;                 for (int m = 0; m < 4; ++m)
; #pragma unroll
;                     for (int n = 0; n < 2; ++n) acc[a][b][m][n] = (f32x4){0.f, 0.f, 0.f, 0.f};
;         cur = nxt; cA = nA; cB = nB; ++ui;
;         if (wr == 1) PG8_BAR;
;     DI void operator()(const f32x4 (&acc)[2][2][4][2], const Unit& u, int wr, int wc, int fr, int fq) const {
;     ...
;             for (int m = 0; m < 4; ++m) { const size_t r = (size_t)(row0 + ai * 128 + m * 16); u32x2 o8v[2];
; #pragma unroll
;                 for (int bj = 0; bj < 2; ++bj) {
;                     const u32x2 gg = g[ai][m][bj];
;                     f32x4 v0 = acc[ai][bj][m][0], v1 = acc[ai][bj][m][1];
;                     v0[0] *= (float)((gg.x >> 0) & 0xffu) * k; v0[1] *= (float)((gg.x >> 8) & 0xffu) * k; v0[2] *= (float)((gg.x >> 16) & 0xffu) * k; v0[3] *= (float)((gg.x >> 24) & 0xffu) * k;
;                     v1[0] *= (float)((gg.y >> 0) & 0xffu) * k; v1[1] *= (float)((gg.y >> 8) & 0xffu) * k; v1[2] *= (float)((gg.y >> 16) & 0xffu) * k; v1[3] *= (float)((gg.y >> 24) & 0xffu) * k;
;                     if (ADD) { const u32x2 o = ov[m][bj]; const f32x2 oa = __builtin_amdgcn_cvt_pk_f32_fp8((int)o.x, false), ob = __builtin_amdgcn_cvt_pk_f32_fp8((int)o.x, true), oc = __builtin_amdgcn_cvt_pk_f32_fp8((int)o.y, false), od = __builtin_amdgcn_cvt_pk_f32_fp8((int)o.y, true);
;                         v0[0] += oa[0]; v0[1] += oa[1]; v0[2] += ob[0]; v0[3] += ob[1]; v1[0] += oc[0]; v1[1] += oc[1]; v1[2] += od[0]; v1[3] += od[1];
;                     }
;                     o8v[bj].x = pk4_fp8(v0[0], v0[1], v0[2], v0[3]); o8v[bj].y = pk4_fp8(v1[0], v1[1], v1[2], v1[3]); }
;                 st_pair16((ADD ? mix8 : (unsigned char*)mix) + r * 1024 + col0, 128, o8v[0], o8v[1], fq); }
	v_med3_f32 v28, v8, s35, v225
	v_med3_f32 v9, v9, s35, v225
	v_mov_b32_e32 v8, v4
	v_cvt_f32_ubyte2_e32 v24, v22
	v_cvt_f32_ubyte3_e32 v22, v22
	v_cvt_pk_fp8_f32 v8, v28, v9
	v_mul_f32_e32 v24, 0x38808081, v24
	v_mul_f32_e32 v22, 0x38808081, v22
	v_cvt_f32_ubyte0_e32 v25, v23
	v_cvt_f32_ubyte1_e32 v26, v23
	v_mul_f32_e32 v24, v60, v24
	v_mul_f32_e32 v22, v61, v22
	v_mul_f32_e32 v25, 0x38808081, v25
	v_mul_f32_e32 v26, 0x38808081, v26
	v_mul_f32_e32 v25, v54, v25
	v_mul_f32_e32 v26, v55, v26
	v_med3_f32 v9, v24, s35, v225
	v_med3_f32 v22, v22, s35, v225
	v_cvt_pk_fp8_f32 v8, v9, v22 op_sel:[0,0,1]
	v_med3_f32 v22, v25, s35, v225
	v_med3_f32 v24, v26, s35, v225
	v_mov_b32_e32 v9, v4
	v_cvt_f32_ubyte2_e32 v27, v23
	v_cvt_f32_ubyte3_e32 v23, v23
	v_cvt_pk_fp8_f32 v9, v22, v24
	v_mul_f32_e32 v27, 0x38808081, v27
	v_mul_f32_e32 v23, 0x38808081, v23
	v_mul_f32_e32 v27, v56, v27
	v_mul_f32_e32 v23, v57, v23
	v_med3_f32 v22, v27, s35, v225
	v_med3_f32 v23, v23, s35, v225
	v_cvt_pk_fp8_f32 v9, v22, v23 op_sel:[0,0,1]
	v_permlane16_swap_b32_e32 v6, v8
	v_lshl_add_u64 v[10:11], v[10:11], 0, v[12:13]
	v_permlane16_swap_b32_e32 v7, v9
	global_store_dwordx4 v[20:21], v[6:9], off
	v_cvt_f32_ubyte1_e32 v20, v19
	v_mul_f32_e32 v20, 0x38808081, v20
	v_cvt_f32_ubyte0_e32 v6, v18
	v_cvt_f32_ubyte1_e32 v7, v18
	v_mul_f32_e32 v6, 0x38808081, v6
	v_mul_f32_e32 v7, 0x38808081, v7
	v_mul_f32_e32 v6, v50, v6
	v_mul_f32_e32 v7, v51, v7
	v_med3_f32 v22, v6, s35, v225
	v_med3_f32 v7, v7, s35, v225
	v_mov_b32_e32 v6, v4
	v_cvt_f32_ubyte2_e32 v8, v18
	v_cvt_f32_ubyte3_e32 v9, v18
	v_cvt_pk_fp8_f32 v6, v22, v7
	v_mul_f32_e32 v8, 0x38808081, v8
	v_mul_f32_e32 v9, 0x38808081, v9
	v_cvt_f32_ubyte0_e32 v18, v19
	v_mul_f32_e32 v8, v52, v8
	v_mul_f32_e32 v9, v53, v9
	v_mul_f32_e32 v18, 0x38808081, v18
	v_mul_f32_e32 v18, v46, v18
	v_mul_f32_e32 v20, v47, v20
	v_med3_f32 v7, v8, s35, v225
	v_med3_f32 v8, v9, s35, v225
	v_cvt_pk_fp8_f32 v6, v7, v8 op_sel:[0,0,1]
	v_med3_f32 v8, v18, s35, v225
	v_med3_f32 v9, v20, s35, v225
	v_mov_b32_e32 v7, v4
	v_cvt_f32_ubyte2_e32 v21, v19
	v_cvt_f32_ubyte3_e32 v19, v19
	v_cvt_pk_fp8_f32 v7, v8, v9
	v_mul_f32_e32 v21, 0x38808081, v21
	v_mul_f32_e32 v19, 0x38808081, v19
	v_mul_f32_e32 v21, v48, v21
	v_mul_f32_e32 v19, v49, v19
	v_med3_f32 v8, v21, s35, v225
	v_med3_f32 v9, v19, s35, v225
	v_cvt_pk_fp8_f32 v7, v8, v9 op_sel:[0,0,1]
	v_cvt_f32_ubyte0_e32 v8, v16
	v_cvt_f32_ubyte1_e32 v9, v16
	v_mul_f32_e32 v8, 0x38808081, v8
	v_mul_f32_e32 v9, 0x38808081, v9
	v_mul_f32_e32 v8, v42, v8
	v_mul_f32_e32 v9, v43, v9
	v_med3_f32 v22, v8, s35, v225
	v_med3_f32 v9, v9, s35, v225
	v_mov_b32_e32 v8, v4
	v_cvt_f32_ubyte2_e32 v18, v16
	v_cvt_f32_ubyte3_e32 v16, v16
	v_cvt_pk_fp8_f32 v8, v22, v9
	v_mul_f32_e32 v18, 0x38808081, v18
	v_mul_f32_e32 v16, 0x38808081, v16
	v_cvt_f32_ubyte0_e32 v19, v17
	v_cvt_f32_ubyte1_e32 v20, v17
	v_mul_f32_e32 v18, v44, v18
	v_mul_f32_e32 v16, v45, v16
	v_mul_f32_e32 v19, 0x38808081, v19
	v_mul_f32_e32 v20, 0x38808081, v20
	v_mul_f32_e32 v19, v38, v19
	v_mul_f32_e32 v20, v39, v20
	v_med3_f32 v9, v18, s35, v225
	v_med3_f32 v16, v16, s35, v225
	v_cvt_pk_fp8_f32 v8, v9, v16 op_sel:[0,0,1]
	v_med3_f32 v16, v19, s35, v225
	v_med3_f32 v18, v20, s35, v225
	v_mov_b32_e32 v9, v4
	v_cvt_f32_ubyte2_e32 v21, v17
	v_cvt_f32_ubyte3_e32 v17, v17
	v_cvt_pk_fp8_f32 v9, v16, v18
	v_mul_f32_e32 v21, 0x38808081, v21
	v_mul_f32_e32 v17, 0x38808081, v17
	v_mul_f32_e32 v21, v40, v21
	v_mul_f32_e32 v17, v41, v17
	v_med3_f32 v16, v21, s35, v225
	v_med3_f32 v17, v17, s35, v225
	v_cvt_pk_fp8_f32 v9, v16, v17 op_sel:[0,0,1]
	v_permlane16_swap_b32_e32 v6, v8
	s_nop 0
	v_permlane16_swap_b32_e32 v7, v9
	global_store_dwordx4 v[10:11], v[6:9], off
	s_cbranch_vccnz .LBB0_895
	s_andn2_b64 vcc, exec, s[16:17]
	s_cbranch_vccnz .LBB0_894
	s_barrier
	s_branch .LBB0_894

; #define GAS __attribute__((address_space(1)))
;     DI void operator()(const f32x4 (&acc)[2][2][4][2], const Unit& u, int wr, int wc, int fr, int fq) const {
;     ...
;         const int row0 = u.pm * 256 + wr * 64 + fr, col0 = u.pn * 256 + wc * 32 + 8 * fq; constexpr float k = W8_INV / 255.0f;
;         u32x2 g[2][4][2];
; #pragma unroll
;         for (int ai = 0; ai < 2; ++ai)
; #pragma unroll
;             for (int m = 0; m < 4; ++m)
; #pragma unroll
;                 for (int bj = 0; bj < 2; ++bj) g[ai][m][bj] = *(const GAS u32x2*)(gt + (size_t)(row0 + ai * 128 + m * 16) * 2048 + col0 + bj * 128);
; #pragma unroll
;         for (int ai = 0; ai < 2; ++ai) {
;             u32x2 ov[4][2];
;             if (ADD) {
; #pragma unroll
;                 for (int m = 0; m < 4; ++m)
; #pragma unroll
;                     for (int bj = 0; bj < 2; ++bj) ov[m][bj] = *(const GAS u32x2*)((const GAS unsigned char*)mix + (size_t)(row0 + ai * 128 + m * 16) * 1024 + col0 + bj * 128);
;             }
;             asm volatile("" ::: "memory");
; #pragma unroll
;             for (int m = 0; m < 4; ++m) { const size_t r = (size_t)(row0 + ai * 128 + m * 16); u32x2 o8v[2];
; #pragma unroll
;                 for (int bj = 0; bj < 2; ++bj) {
;                     const u32x2 gg = g[ai][m][bj];
;                     f32x4 v0 = acc[ai][bj][m][0], v1 = acc[ai][bj][m][1];
;                     v0[0] *= (float)((gg.x >> 0) & 0xffu) * k; v0[1] *= (float)((gg.x >> 8) & 0xffu) * k; v0[2] *= (float)((gg.x >> 16) & 0xffu) * k; v0[3] *= (float)((gg.x >> 24) & 0xffu) * k;
;                     v1[0] *= (float)((gg.y >> 0) & 0xffu) * k; v1[1] *= (float)((gg.y >> 8) & 0xffu) * k; v1[2] *= (float)((gg.y >> 16) & 0xffu) * k; v1[3] *= (float)((gg.y >> 24) & 0xffu) * k;
;                     if (ADD) { const u32x2 o = ov[m][bj]; const f32x2 oa = __builtin_amdgcn_cvt_pk_f32_fp8((int)o.x, false), ob = __builtin_amdgcn_cvt_pk_f32_fp8((int)o.x, true), oc = __builtin_amdgcn_cvt_pk_f32_fp8((int)o.y, false), od = __builtin_amdgcn_cvt_pk_f32_fp8((int)o.y, true);
;                         v0[0] += oa[0]; v0[1] += oa[1]; v0[2] += ob[0]; v0[3] += ob[1]; v1[0] += oc[0]; v1[1] += oc[1]; v1[2] += od[0]; v1[3] += od[1];
;                     }
;                     o8v[bj].x = pk4_fp8(v0[0], v0[1], v0[2], v0[3]); o8v[bj].y = pk4_fp8(v1[0], v1[1], v1[2], v1[3]); }
.LBB0_975:
	s_lshl_b32 s6, s58, 8
	v_mov_b32_e32 v144, v1
	v_mov_b32_e32 v154, v5
	s_add_i32 s6, s6, s86
	s_nop 15
	s_andn2_b64 vcc, exec, s[40:41]
	v_add_u32_e32 v146, s6, v144
	s_lshl_b32 s6, s97, 8
	s_or_b32 s6, s6, s87
	v_lshl_add_u32 v144, v154, 3, s6
	v_ashrrev_i32_e32 v145, 31, v144
	v_ashrrev_i32_e32 v147, 31, v146
	v_lshl_add_u64 v[148:149], s[42:43], 0, v[144:145]
	v_lshlrev_b64 v[150:151], 11, v[146:147]
	v_lshl_add_u64 v[150:151], v[148:149], 0, v[150:151]
	global_load_dwordx2 v[198:199], v[150:151], off
	v_lshl_add_u64 v[162:163], s[30:31], 0, v[144:145]
	v_lshlrev_b64 v[200:201], 10, v[146:147]
	v_lshl_add_u64 v[152:153], v[162:163], 0, v[200:201]
	global_load_dwordx2 v[212:213], v[152:153], off
	global_load_dwordx2 v[216:217], v[152:153], off offset:128
	global_load_dwordx2 v[214:215], v[150:151], off offset:128
	v_bfe_i32 v155, v154, 0, 1
	v_add_u32_e32 v154, 16, v146
	v_add_u32_e32 v156, 32, v146
	v_add_u32_e32 v158, 48, v146
	v_add_u32_e32 v174, 0x80, v146
	v_add_u32_e32 v168, 0x90, v146
	v_add_u32_e32 v166, 0xa0, v146
	v_add_u32_e32 v164, 0xb0, v146
	v_and_b32_e32 v146, 0x78, v155
	v_ashrrev_i32_e32 v155, 31, v154
	v_ashrrev_i32_e32 v157, 31, v156
	v_ashrrev_i32_e32 v159, 31, v158
	v_ashrrev_i32_e32 v175, 31, v174
	v_ashrrev_i32_e32 v169, 31, v168
	v_ashrrev_i32_e32 v167, 31, v166
	v_ashrrev_i32_e32 v165, 31, v164
	v_lshlrev_b64 v[160:161], 11, v[154:155]
	v_lshlrev_b64 v[170:171], 11, v[156:157]
	v_lshlrev_b64 v[176:177], 11, v[158:159]
	v_lshlrev_b64 v[178:179], 11, v[174:175]
	v_lshlrev_b64 v[180:181], 11, v[168:169]
	v_lshlrev_b64 v[150:151], 11, v[166:167]
	v_lshlrev_b64 v[182:183], 11, v[164:165]
	v_lshlrev_b64 v[192:193], 10, v[154:155]
	v_lshlrev_b64 v[184:185], 10, v[156:157]
	v_lshlrev_b64 v[172:173], 10, v[158:159]
	v_lshl_add_u64 v[154:155], v[148:149], 0, v[160:161]
	v_lshl_add_u64 v[156:157], v[148:149], 0, v[170:171]
	v_lshl_add_u64 v[158:159], v[148:149], 0, v[176:177]
	v_lshl_add_u64 v[160:161], v[148:149], 0, v[178:179]
	v_lshl_add_u64 v[178:179], v[148:149], 0, v[180:181]
	v_lshl_add_u64 v[150:151], v[148:149], 0, v[150:151]
	v_lshl_add_u64 v[148:149], v[148:149], 0, v[182:183]
	v_lshl_add_u64 v[182:183], v[162:163], 0, v[192:193]
	v_lshl_add_u64 v[188:189], v[162:163], 0, v[184:185]
	v_lshl_add_u64 v[218:219], v[162:163], 0, v[172:173]
	global_load_dwordx2 v[220:221], v[154:155], off
	global_load_dwordx2 v[226:227], v[154:155], off offset:128
	global_load_dwordx2 v[190:191], v[156:157], off
	global_load_dwordx2 v[186:187], v[156:157], off offset:128
	global_load_dwordx2 v[180:181], v[158:159], off
	global_load_dwordx2 v[176:177], v[158:159], off offset:128
	global_load_dwordx2 v[170:171], v[160:161], off
	s_nop 0
	global_load_dwordx2 v[160:161], v[160:161], off offset:128
	s_nop 0
	global_load_dwordx2 v[158:159], v[178:179], off
	global_load_dwordx2 v[156:157], v[178:179], off offset:128
	global_load_dwordx2 v[154:155], v[150:151], off
	global_load_dwordx2 v[152:153], v[150:151], off offset:128
	s_nop 0
	global_load_dwordx2 v[150:151], v[148:149], off
	s_nop 0
	global_load_dwordx2 v[148:149], v[148:149], off offset:128
	s_nop 0
	global_load_dwordx2 v[228:229], v[182:183], off
	global_load_dwordx2 v[230:231], v[182:183], off offset:128
	global_load_dwordx2 v[194:195], v[188:189], off
	s_nop 0
	global_load_dwordx2 v[188:189], v[188:189], off offset:128
	s_nop 0
	global_load_dwordx2 v[182:183], v[218:219], off
	global_load_dwordx2 v[178:179], v[218:219], off offset:128
	v_mov_b32_e32 v147, v4
	s_mov_b64 s[40:41], -1
	s_waitcnt vmcnt(0)
	v_cvt_f32_ubyte0_e32 v203, v198
	v_cvt_f32_ubyte1_e32 v206, v198
	v_cvt_f32_ubyte2_e32 v218, v198
	v_cvt_f32_ubyte3_e32 v198, v198
	v_mul_f32_e32 v236, 0x38808081, v198
	v_cvt_f32_ubyte0_e32 v198, v199
	v_mul_f32_e32 v237, 0x38808081, v198
	v_cvt_f32_ubyte1_e32 v198, v199
	v_mul_f32_e32 v238, 0x38808081, v198
	v_cvt_f32_ubyte2_e32 v198, v199
	v_mul_f32_e32 v239, 0x38808081, v198
	v_cvt_f32_ubyte3_e32 v198, v199
	v_mul_f32_e32 v240, 0x38808081, v198
	v_cvt_pk_f32_fp8_e32 v[198:199], v212
	v_mul_f32_e32 v235, 0x38808081, v218
	v_cvt_pk_f32_fp8_sdwa v[218:219], v212 src0_sel:WORD_1
	v_cvt_pk_f32_fp8_e32 v[232:233], v213
	v_cvt_pk_f32_fp8_sdwa v[212:213], v213 src0_sel:WORD_1
	v_mul_f32_e32 v203, 0x38808081, v203
	v_mul_f32_e32 v206, 0x38808081, v206
	v_fma_f32 v130, v130, v203, v198
	v_fmac_f32_e32 v199, v131, v206
	v_fma_f32 v131, v132, v235, v218
	v_fma_f32 v132, v126, v237, v232
	v_fmac_f32_e32 v233, v127, v238
	v_fmac_f32_e32 v213, v129, v240
	v_med3_f32 v127, v130, s35, v225
	v_med3_f32 v129, v199, s35, v225
	v_mov_b32_e32 v126, v4
	v_cvt_pk_fp8_f32 v126, v127, v129
	v_med3_f32 v129, v131, s35, v225
	v_med3_f32 v131, v132, s35, v225
	v_med3_f32 v132, v233, s35, v225
	v_mov_b32_e32 v127, v4
	v_cvt_pk_fp8_f32 v127, v131, v132
	v_fmac_f32_e32 v219, v133, v236
	v_fma_f32 v128, v128, v239, v212
	v_med3_f32 v130, v219, s35, v225
	v_cvt_pk_fp8_f32 v126, v129, v130 op_sel:[0,0,1]
	v_med3_f32 v128, v128, s35, v225
	v_med3_f32 v129, v213, s35, v225
	v_cvt_pk_fp8_f32 v127, v128, v129 op_sel:[0,0,1]
	v_cvt_f32_ubyte0_e32 v128, v214
	v_mul_f32_e32 v203, 0x38808081, v128
	v_cvt_f32_ubyte1_e32 v128, v214
	v_mul_f32_e32 v206, 0x38808081, v128
	v_cvt_f32_ubyte2_e32 v128, v214
	v_mul_f32_e32 v212, 0x38808081, v128
	v_cvt_f32_ubyte3_e32 v128, v214
	v_mul_f32_e32 v213, 0x38808081, v128
	v_cvt_f32_ubyte0_e32 v128, v215
	v_mul_f32_e32 v214, 0x38808081, v128
	v_cvt_f32_ubyte1_e32 v128, v215
	v_mul_f32_e32 v218, 0x38808081, v128
	v_cvt_f32_ubyte2_e32 v128, v215
	v_mul_f32_e32 v219, 0x38808081, v128
	v_cvt_f32_ubyte3_e32 v128, v215
	v_mul_f32_e32 v215, 0x38808081, v128
	v_cvt_pk_f32_fp8_e32 v[128:129], v216
; DI unsigned pk4_fp8(float a, float b, float c_, float d) { int w = 0; w = __builtin_amdgcn_cvt_pk_fp8_f32(clamp8(a), clamp8(b), w, false); w = __builtin_amdgcn_cvt_pk_fp8_f32(clamp8(c_), clamp8(d), w, true); return (unsigned)w; }
;     DI void operator()(const f32x4 (&acc)[2][2][4][2], const Unit& u, int wr, int wc, int fr, int fq) const {
;     ...
;             for (int m = 0; m < 4; ++m) { const size_t r = (size_t)(row0 + ai * 128 + m * 16); u32x2 o8v[2];
; #pragma unroll
;                 for (int bj = 0; bj < 2; ++bj) {
;                     const u32x2 gg = g[ai][m][bj];
;                     f32x4 v0 = acc[ai][bj][m][0], v1 = acc[ai][bj][m][1];
;                     v0[0] *= (float)((gg.x >> 0) & 0xffu) * k; v0[1] *= (float)((gg.x >> 8) & 0xffu) * k; v0[2] *= (float)((gg.x >> 16) & 0xffu) * k; v0[3] *= (float)((gg.x >> 24) & 0xffu) * k;
;                     v1[0] *= (float)((gg.y >> 0) & 0xffu) * k; v1[1] *= (float)((gg.y >> 8) & 0xffu) * k; v1[2] *= (float)((gg.y >> 16) & 0xffu) * k; v1[3] *= (float)((gg.y >> 24) & 0xffu) * k;
;                     if (ADD) { const u32x2 o = ov[m][bj]; const f32x2 oa = __builtin_amdgcn_cvt_pk_f32_fp8((int)o.x, false), ob = __builtin_amdgcn_cvt_pk_f32_fp8((int)o.x, true), oc = __builtin_amdgcn_cvt_pk_f32_fp8((int)o.y, false), od = __builtin_amdgcn_cvt_pk_f32_fp8((int)o.y, true);
;                         v0[0] += oa[0]; v0[1] += oa[1]; v0[2] += ob[0]; v0[3] += ob[1]; v1[0] += oc[0]; v1[1] += oc[1]; v1[2] += od[0]; v1[3] += od[1];
;                     }
;                     o8v[bj].x = pk4_fp8(v0[0], v0[1], v0[2], v0[3]); o8v[bj].y = pk4_fp8(v1[0], v1[1], v1[2], v1[3]); }
;                 st_pair16((ADD ? mix8 : (unsigned char*)mix) + r * 1024 + col0, 128, o8v[0], o8v[1], fq); }
	v_cvt_pk_f32_fp8_e32 v[132:133], v217
	v_cvt_pk_f32_fp8_sdwa v[198:199], v217 src0_sel:WORD_1
	v_cvt_pk_f32_fp8_sdwa v[130:131], v216 src0_sel:WORD_1
	v_fma_f32 v122, v122, v203, v128
	v_fmac_f32_e32 v129, v123, v206
	v_fma_f32 v118, v118, v214, v132
	v_fmac_f32_e32 v133, v119, v218
	v_fma_f32 v119, v120, v219, v198
	v_fmac_f32_e32 v199, v121, v215
	v_med3_f32 v120, v122, s35, v225
	v_med3_f32 v121, v129, s35, v225
	v_mov_b32_e32 v128, v4
	v_med3_f32 v118, v118, s35, v225
	v_med3_f32 v122, v133, s35, v225
	v_mov_b32_e32 v129, v4
	v_cvt_pk_fp8_f32 v128, v120, v121
	v_cvt_pk_fp8_f32 v129, v118, v122
	v_fma_f32 v123, v124, v212, v130
	v_fmac_f32_e32 v131, v125, v213
	v_med3_f32 v120, v123, s35, v225
	v_med3_f32 v121, v131, s35, v225
	v_med3_f32 v118, v119, s35, v225
	v_med3_f32 v119, v199, s35, v225
	v_cvt_pk_fp8_f32 v128, v120, v121 op_sel:[0,0,1]
	v_cvt_pk_fp8_f32 v129, v118, v119 op_sel:[0,0,1]
	v_lshl_add_u64 v[118:119], s[44:45], 0, v[200:201]
	v_lshl_add_u64 v[118:119], v[118:119], 0, v[144:145]
	v_permlane16_swap_b32_e32 v126, v128
	v_permlane16_swap_b32_e32 v127, v129
	v_lshl_add_u64 v[118:119], v[118:119], 0, v[146:147]
	global_store_dwordx4 v[118:119], v[126:129], off
	v_cvt_f32_ubyte0_e32 v118, v220
	v_cvt_pk_f32_fp8_sdwa v[120:121], v228 src0_sel:WORD_1
	v_mul_f32_e32 v126, 0x38808081, v118
	v_cvt_f32_ubyte1_e32 v118, v220
	v_mul_f32_e32 v127, 0x38808081, v118
	v_cvt_f32_ubyte2_e32 v118, v220
	v_mul_f32_e32 v128, 0x38808081, v118
	v_cvt_f32_ubyte3_e32 v118, v220
	v_mul_f32_e32 v129, 0x38808081, v118
	v_cvt_f32_ubyte0_e32 v118, v221
	v_mul_f32_e32 v130, 0x38808081, v118
	v_cvt_f32_ubyte1_e32 v118, v221
	v_mul_f32_e32 v131, 0x38808081, v118
	v_cvt_f32_ubyte2_e32 v118, v221
	v_mul_f32_e32 v132, 0x38808081, v118
	v_cvt_f32_ubyte3_e32 v118, v221
	v_mul_f32_e32 v133, 0x38808081, v118
	v_cvt_pk_f32_fp8_e32 v[118:119], v228
	v_cvt_pk_f32_fp8_e32 v[122:123], v229
	v_cvt_pk_f32_fp8_sdwa v[124:125], v229 src0_sel:WORD_1
	v_fmac_f32_e32 v121, v117, v129
	v_fma_f32 v114, v114, v126, v118
	v_fmac_f32_e32 v119, v115, v127
	v_fma_f32 v115, v116, v128, v120
	v_fma_f32 v116, v110, v130, v122
	v_fmac_f32_e32 v123, v111, v131
	v_fmac_f32_e32 v125, v113, v133
	v_med3_f32 v111, v114, s35, v225
	v_med3_f32 v113, v119, s35, v225
	v_mov_b32_e32 v110, v4
	v_cvt_pk_fp8_f32 v110, v111, v113
	v_med3_f32 v113, v115, s35, v225
	v_med3_f32 v115, v116, s35, v225
	v_med3_f32 v116, v123, s35, v225
	v_mov_b32_e32 v111, v4
	v_cvt_pk_fp8_f32 v111, v115, v116
	v_fma_f32 v112, v112, v132, v124
	v_med3_f32 v114, v121, s35, v225
	v_cvt_pk_fp8_f32 v110, v113, v114 op_sel:[0,0,1]
	v_med3_f32 v112, v112, s35, v225
	v_med3_f32 v113, v125, s35, v225
	v_cvt_pk_fp8_f32 v111, v112, v113 op_sel:[0,0,1]
	v_cvt_f32_ubyte0_e32 v112, v226
	v_mul_f32_e32 v120, 0x38808081, v112
	v_cvt_f32_ubyte1_e32 v112, v226
	v_mul_f32_e32 v121, 0x38808081, v112
	v_cvt_f32_ubyte2_e32 v112, v226
	v_mul_f32_e32 v122, 0x38808081, v112
	v_cvt_f32_ubyte3_e32 v112, v226
	v_mul_f32_e32 v123, 0x38808081, v112
	v_cvt_f32_ubyte0_e32 v112, v227
	v_mul_f32_e32 v124, 0x38808081, v112
	v_cvt_f32_ubyte1_e32 v112, v227
	v_mul_f32_e32 v125, 0x38808081, v112
	v_cvt_f32_ubyte2_e32 v112, v227
	v_mul_f32_e32 v126, 0x38808081, v112
	v_cvt_f32_ubyte3_e32 v112, v227
	v_mul_f32_e32 v127, 0x38808081, v112
	v_cvt_pk_f32_fp8_e32 v[112:113], v230
	v_cvt_pk_f32_fp8_e32 v[116:117], v231
	v_cvt_pk_f32_fp8_sdwa v[118:119], v231 src0_sel:WORD_1
	v_cvt_pk_f32_fp8_sdwa v[114:115], v230 src0_sel:WORD_1
	v_fma_f32 v106, v106, v120, v112
	v_fmac_f32_e32 v113, v107, v121
	v_fma_f32 v102, v102, v124, v116
	v_fmac_f32_e32 v117, v103, v125
	v_fma_f32 v103, v104, v126, v118
	v_fmac_f32_e32 v119, v105, v127
	v_med3_f32 v104, v106, s35, v225
	v_med3_f32 v105, v113, s35, v225
	v_mov_b32_e32 v112, v4
	v_med3_f32 v102, v102, s35, v225
	v_med3_f32 v106, v117, s35, v225
	v_mov_b32_e32 v113, v4
	v_cvt_pk_fp8_f32 v112, v104, v105
	v_cvt_pk_fp8_f32 v113, v102, v106
	v_fma_f32 v107, v108, v122, v114
	v_fmac_f32_e32 v115, v109, v123
	v_med3_f32 v104, v107, s35, v225
	v_med3_f32 v105, v115, s35, v225
	v_med3_f32 v102, v103, s35, v225
	v_med3_f32 v103, v119, s35, v225
	v_cvt_pk_fp8_f32 v112, v104, v105 op_sel:[0,0,1]
	v_cvt_pk_fp8_f32 v113, v102, v103 op_sel:[0,0,1]
	v_lshl_add_u64 v[102:103], s[44:45], 0, v[192:193]
	v_lshl_add_u64 v[102:103], v[102:103], 0, v[144:145]
	v_permlane16_swap_b32_e32 v110, v112
	v_permlane16_swap_b32_e32 v111, v113
	v_lshl_add_u64 v[102:103], v[102:103], 0, v[146:147]
	global_store_dwordx4 v[102:103], v[110:113], off
	v_cvt_f32_ubyte0_e32 v102, v190
	v_cvt_pk_f32_fp8_sdwa v[104:105], v194 src0_sel:WORD_1
	v_mul_f32_e32 v110, 0x38808081, v102
	v_cvt_f32_ubyte1_e32 v102, v190
	v_mul_f32_e32 v111, 0x38808081, v102
	v_cvt_f32_ubyte2_e32 v102, v190
	v_mul_f32_e32 v112, 0x38808081, v102
	v_cvt_f32_ubyte3_e32 v102, v190
	v_mul_f32_e32 v113, 0x38808081, v102
	v_cvt_f32_ubyte0_e32 v102, v191
	v_mul_f32_e32 v114, 0x38808081, v102
	v_cvt_f32_ubyte1_e32 v102, v191
	v_mul_f32_e32 v115, 0x38808081, v102
	v_cvt_f32_ubyte2_e32 v102, v191
	v_mul_f32_e32 v116, 0x38808081, v102
	v_cvt_f32_ubyte3_e32 v102, v191
	v_mul_f32_e32 v117, 0x38808081, v102
	v_cvt_pk_f32_fp8_e32 v[102:103], v194
	v_cvt_pk_f32_fp8_e32 v[106:107], v195
	v_cvt_pk_f32_fp8_sdwa v[108:109], v195 src0_sel:WORD_1
	v_fmac_f32_e32 v105, v101, v113
	v_fma_f32 v98, v98, v110, v102
	v_fmac_f32_e32 v103, v99, v111
	v_fma_f32 v99, v100, v112, v104
	v_fma_f32 v100, v94, v114, v106
	v_fmac_f32_e32 v107, v95, v115
	v_fmac_f32_e32 v109, v97, v117
	v_med3_f32 v95, v98, s35, v225
	v_med3_f32 v97, v103, s35, v225
	v_mov_b32_e32 v94, v4
	v_cvt_pk_fp8_f32 v94, v95, v97
	v_med3_f32 v97, v99, s35, v225
; #define GAS __attribute__((address_space(1)))
; DI unsigned pk4_fp8(float a, float b, float c_, float d) { int w = 0; w = __builtin_amdgcn_cvt_pk_fp8_f32(clamp8(a), clamp8(b), w, false); w = __builtin_amdgcn_cvt_pk_fp8_f32(clamp8(c_), clamp8(d), w, true); return (unsigned)w; }
;     DI void operator()(const f32x4 (&acc)[2][2][4][2], const Unit& u, int wr, int wc, int fr, int fq) const {
;     ...
;                     for (int bj = 0; bj < 2; ++bj) ov[m][bj] = *(const GAS u32x2*)((const GAS unsigned char*)mix + (size_t)(row0 + ai * 128 + m * 16) * 1024 + col0 + bj * 128);
;             }
;             asm volatile("" ::: "memory");
; #pragma unroll
;             for (int m = 0; m < 4; ++m) { const size_t r = (size_t)(row0 + ai * 128 + m * 16); u32x2 o8v[2];
; #pragma unroll
;                 for (int bj = 0; bj < 2; ++bj) {
;                     const u32x2 gg = g[ai][m][bj];
;                     f32x4 v0 = acc[ai][bj][m][0], v1 = acc[ai][bj][m][1];
;                     v0[0] *= (float)((gg.x >> 0) & 0xffu) * k; v0[1] *= (float)((gg.x >> 8) & 0xffu) * k; v0[2] *= (float)((gg.x >> 16) & 0xffu) * k; v0[3] *= (float)((gg.x >> 24) & 0xffu) * k;
;                     v1[0] *= (float)((gg.y >> 0) & 0xffu) * k; v1[1] *= (float)((gg.y >> 8) & 0xffu) * k; v1[2] *= (float)((gg.y >> 16) & 0xffu) * k; v1[3] *= (float)((gg.y >> 24) & 0xffu) * k;
;                     if (ADD) { const u32x2 o = ov[m][bj]; const f32x2 oa = __builtin_amdgcn_cvt_pk_f32_fp8((int)o.x, false), ob = __builtin_amdgcn_cvt_pk_f32_fp8((int)o.x, true), oc = __builtin_amdgcn_cvt_pk_f32_fp8((int)o.y, false), od = __builtin_amdgcn_cvt_pk_f32_fp8((int)o.y, true);
;                         v0[0] += oa[0]; v0[1] += oa[1]; v0[2] += ob[0]; v0[3] += ob[1]; v1[0] += oc[0]; v1[1] += oc[1]; v1[2] += od[0]; v1[3] += od[1];
;                     }
;                     o8v[bj].x = pk4_fp8(v0[0], v0[1], v0[2], v0[3]); o8v[bj].y = pk4_fp8(v1[0], v1[1], v1[2], v1[3]); }
;                 st_pair16((ADD ? mix8 : (unsigned char*)mix) + r * 1024 + col0, 128, o8v[0], o8v[1], fq); }
	v_med3_f32 v99, v100, s35, v225
	v_med3_f32 v100, v107, s35, v225
	v_mov_b32_e32 v95, v4
	v_cvt_pk_fp8_f32 v95, v99, v100
	v_fma_f32 v96, v96, v116, v108
	v_med3_f32 v98, v105, s35, v225
	v_cvt_pk_fp8_f32 v94, v97, v98 op_sel:[0,0,1]
	v_med3_f32 v96, v96, s35, v225
	v_med3_f32 v97, v109, s35, v225
	v_cvt_pk_fp8_f32 v95, v96, v97 op_sel:[0,0,1]
	v_cvt_f32_ubyte0_e32 v96, v186
	v_mul_f32_e32 v104, 0x38808081, v96
	v_cvt_f32_ubyte1_e32 v96, v186
	v_mul_f32_e32 v105, 0x38808081, v96
	v_cvt_f32_ubyte2_e32 v96, v186
	v_mul_f32_e32 v106, 0x38808081, v96
	v_cvt_f32_ubyte3_e32 v96, v186
	v_mul_f32_e32 v107, 0x38808081, v96
	v_cvt_f32_ubyte0_e32 v96, v187
	v_mul_f32_e32 v108, 0x38808081, v96
	v_cvt_f32_ubyte1_e32 v96, v187
	v_mul_f32_e32 v109, 0x38808081, v96
	v_cvt_f32_ubyte2_e32 v96, v187
	v_mul_f32_e32 v110, 0x38808081, v96
	v_cvt_f32_ubyte3_e32 v96, v187
	v_mul_f32_e32 v111, 0x38808081, v96
	v_cvt_pk_f32_fp8_e32 v[96:97], v188
	v_cvt_pk_f32_fp8_e32 v[100:101], v189
	v_cvt_pk_f32_fp8_sdwa v[102:103], v189 src0_sel:WORD_1
	v_cvt_pk_f32_fp8_sdwa v[98:99], v188 src0_sel:WORD_1
	v_fma_f32 v90, v90, v104, v96
	v_fmac_f32_e32 v97, v91, v105
	v_fma_f32 v86, v86, v108, v100
	v_fmac_f32_e32 v101, v87, v109
	v_fma_f32 v87, v88, v110, v102
	v_fmac_f32_e32 v103, v89, v111
	v_med3_f32 v88, v90, s35, v225
	v_med3_f32 v89, v97, s35, v225
	v_mov_b32_e32 v96, v4
	v_med3_f32 v86, v86, s35, v225
	v_med3_f32 v90, v101, s35, v225
	v_mov_b32_e32 v97, v4
	v_cvt_pk_fp8_f32 v96, v88, v89
	v_cvt_pk_fp8_f32 v97, v86, v90
	v_fma_f32 v91, v92, v106, v98
	v_fmac_f32_e32 v99, v93, v107
	v_med3_f32 v88, v91, s35, v225
	v_med3_f32 v89, v99, s35, v225
	v_med3_f32 v86, v87, s35, v225
	v_med3_f32 v87, v103, s35, v225
	v_cvt_pk_fp8_f32 v96, v88, v89 op_sel:[0,0,1]
	v_cvt_pk_fp8_f32 v97, v86, v87 op_sel:[0,0,1]
	v_lshl_add_u64 v[86:87], s[44:45], 0, v[184:185]
	v_lshl_add_u64 v[86:87], v[86:87], 0, v[144:145]
	v_permlane16_swap_b32_e32 v94, v96
	v_permlane16_swap_b32_e32 v95, v97
	v_lshl_add_u64 v[86:87], v[86:87], 0, v[146:147]
	global_store_dwordx4 v[86:87], v[94:97], off
	v_cvt_f32_ubyte0_e32 v86, v180
	v_cvt_pk_f32_fp8_sdwa v[88:89], v182 src0_sel:WORD_1
	v_mul_f32_e32 v94, 0x38808081, v86
	v_cvt_f32_ubyte1_e32 v86, v180
	v_mul_f32_e32 v95, 0x38808081, v86
	v_cvt_f32_ubyte2_e32 v86, v180
	v_mul_f32_e32 v96, 0x38808081, v86
	v_cvt_f32_ubyte3_e32 v86, v180
	v_mul_f32_e32 v97, 0x38808081, v86
	v_cvt_f32_ubyte0_e32 v86, v181
	v_mul_f32_e32 v98, 0x38808081, v86
	v_cvt_f32_ubyte1_e32 v86, v181
	v_mul_f32_e32 v99, 0x38808081, v86
	v_cvt_f32_ubyte2_e32 v86, v181
	v_mul_f32_e32 v100, 0x38808081, v86
	v_cvt_f32_ubyte3_e32 v86, v181
	v_mul_f32_e32 v101, 0x38808081, v86
	v_cvt_pk_f32_fp8_e32 v[86:87], v182
	v_cvt_pk_f32_fp8_e32 v[90:91], v183
	v_cvt_pk_f32_fp8_sdwa v[92:93], v183 src0_sel:WORD_1
	v_fmac_f32_e32 v89, v85, v97
	v_fma_f32 v82, v82, v94, v86
	v_fmac_f32_e32 v87, v83, v95
	v_fma_f32 v83, v84, v96, v88
	v_fma_f32 v84, v78, v98, v90
	v_fmac_f32_e32 v91, v79, v99
	v_fmac_f32_e32 v93, v81, v101
	v_med3_f32 v79, v82, s35, v225
	v_med3_f32 v81, v87, s35, v225
	v_mov_b32_e32 v78, v4
	v_cvt_pk_fp8_f32 v78, v79, v81
	v_med3_f32 v81, v83, s35, v225
	v_med3_f32 v82, v89, s35, v225
	v_med3_f32 v83, v84, s35, v225
	v_med3_f32 v84, v91, s35, v225
	v_mov_b32_e32 v79, v4
	v_cvt_pk_fp8_f32 v79, v83, v84
	v_cvt_pk_fp8_f32 v78, v81, v82 op_sel:[0,0,1]
	v_lshlrev_b64 v[82:83], 10, v[174:175]
	v_lshl_add_u64 v[84:85], v[162:163], 0, v[82:83]
	global_load_dwordx2 v[86:87], v[84:85], off
	v_fma_f32 v80, v80, v100, v92
	v_med3_f32 v80, v80, s35, v225
	v_med3_f32 v81, v93, s35, v225
	v_cvt_pk_fp8_f32 v79, v80, v81 op_sel:[0,0,1]
	v_cvt_f32_ubyte0_e32 v80, v176
	global_load_dwordx2 v[84:85], v[84:85], off offset:128
	v_mul_f32_e32 v94, 0x38808081, v80
	v_cvt_f32_ubyte1_e32 v80, v176
	v_mul_f32_e32 v95, 0x38808081, v80
	v_cvt_f32_ubyte2_e32 v80, v176
	v_mul_f32_e32 v96, 0x38808081, v80
	v_cvt_f32_ubyte3_e32 v80, v176
	v_mul_f32_e32 v97, 0x38808081, v80
	v_cvt_f32_ubyte0_e32 v80, v177
	v_mul_f32_e32 v98, 0x38808081, v80
	v_cvt_f32_ubyte1_e32 v80, v177
	v_mul_f32_e32 v99, 0x38808081, v80
	v_cvt_f32_ubyte2_e32 v80, v177
	v_mul_f32_e32 v100, 0x38808081, v80
	v_cvt_f32_ubyte3_e32 v80, v177
	v_mul_f32_e32 v101, 0x38808081, v80
	v_cvt_pk_f32_fp8_e32 v[80:81], v178
	v_cvt_pk_f32_fp8_e32 v[90:91], v179
	v_cvt_pk_f32_fp8_sdwa v[92:93], v179 src0_sel:WORD_1
	v_cvt_pk_f32_fp8_sdwa v[88:89], v178 src0_sel:WORD_1
	v_fma_f32 v66, v66, v94, v80
	v_fmac_f32_e32 v81, v67, v95
	v_fma_f32 v62, v62, v98, v90
	v_fmac_f32_e32 v91, v63, v99
	v_fma_f32 v63, v64, v100, v92
	v_fmac_f32_e32 v93, v65, v101
	v_med3_f32 v64, v66, s35, v225
	v_med3_f32 v65, v81, s35, v225
	v_mov_b32_e32 v80, v4
	v_med3_f32 v62, v62, s35, v225
	v_med3_f32 v66, v91, s35, v225
	v_mov_b32_e32 v81, v4
	v_cvt_pk_fp8_f32 v80, v64, v65
	v_cvt_pk_fp8_f32 v81, v62, v66
	v_fma_f32 v67, v68, v96, v88
	v_fmac_f32_e32 v89, v69, v97
	v_med3_f32 v64, v67, s35, v225
	v_med3_f32 v65, v89, s35, v225
	v_med3_f32 v62, v63, s35, v225
	v_med3_f32 v63, v93, s35, v225
	v_cvt_pk_fp8_f32 v80, v64, v65 op_sel:[0,0,1]
	v_cvt_pk_fp8_f32 v81, v62, v63 op_sel:[0,0,1]
	v_lshl_add_u64 v[62:63], s[44:45], 0, v[172:173]
	v_lshl_add_u64 v[62:63], v[62:63], 0, v[144:145]
	v_permlane16_swap_b32_e32 v78, v80
	v_permlane16_swap_b32_e32 v79, v81
	v_lshl_add_u64 v[62:63], v[62:63], 0, v[146:147]
	v_lshlrev_b64 v[88:89], 10, v[168:169]
	global_store_dwordx4 v[62:63], v[78:81], off
	v_lshl_add_u64 v[62:63], v[162:163], 0, v[88:89]
	global_load_dwordx2 v[90:91], v[62:63], off
	global_load_dwordx2 v[92:93], v[62:63], off offset:128
	v_lshlrev_b64 v[68:69], 10, v[166:167]
	v_lshlrev_b64 v[62:63], 10, v[164:165]
	v_lshl_add_u64 v[64:65], v[162:163], 0, v[68:69]
	v_lshl_add_u64 v[94:95], v[162:163], 0, v[62:63]
	global_load_dwordx2 v[80:81], v[64:65], off
	global_load_dwordx2 v[78:79], v[64:65], off offset:128
	global_load_dwordx2 v[66:67], v[94:95], off
	s_nop 0
	global_load_dwordx2 v[64:65], v[94:95], off offset:128
	v_cvt_f32_ubyte0_e32 v94, v170
	v_mul_f32_e32 v100, 0x38808081, v94
	v_cvt_f32_ubyte1_e32 v94, v170
	v_mul_f32_e32 v101, 0x38808081, v94
	v_cvt_f32_ubyte2_e32 v94, v170
	v_mul_f32_e32 v102, 0x38808081, v94
	v_cvt_f32_ubyte3_e32 v94, v170
	v_mul_f32_e32 v103, 0x38808081, v94
	v_cvt_f32_ubyte0_e32 v94, v171
	v_mul_f32_e32 v104, 0x38808081, v94
	v_cvt_f32_ubyte1_e32 v94, v171
	v_mul_f32_e32 v105, 0x38808081, v94
	v_cvt_f32_ubyte2_e32 v94, v171
	v_mul_f32_e32 v106, 0x38808081, v94
	v_cvt_f32_ubyte3_e32 v94, v171
	v_mul_f32_e32 v107, 0x38808081, v94
	s_waitcnt vmcnt(8)
; DI unsigned pk4_fp8(float a, float b, float c_, float d) { int w = 0; w = __builtin_amdgcn_cvt_pk_fp8_f32(clamp8(a), clamp8(b), w, false); w = __builtin_amdgcn_cvt_pk_fp8_f32(clamp8(c_), clamp8(d), w, true); return (unsigned)w; }
;     DI void operator()(const f32x4 (&acc)[2][2][4][2], const Unit& u, int wr, int wc, int fr, int fq) const {
;     ...
;             for (int m = 0; m < 4; ++m) { const size_t r = (size_t)(row0 + ai * 128 + m * 16); u32x2 o8v[2];
; #pragma unroll
;                 for (int bj = 0; bj < 2; ++bj) {
;                     const u32x2 gg = g[ai][m][bj];
;                     f32x4 v0 = acc[ai][bj][m][0], v1 = acc[ai][bj][m][1];
;                     v0[0] *= (float)((gg.x >> 0) & 0xffu) * k; v0[1] *= (float)((gg.x >> 8) & 0xffu) * k; v0[2] *= (float)((gg.x >> 16) & 0xffu) * k; v0[3] *= (float)((gg.x >> 24) & 0xffu) * k;
;                     v1[0] *= (float)((gg.y >> 0) & 0xffu) * k; v1[1] *= (float)((gg.y >> 8) & 0xffu) * k; v1[2] *= (float)((gg.y >> 16) & 0xffu) * k; v1[3] *= (float)((gg.y >> 24) & 0xffu) * k;
;                     if (ADD) { const u32x2 o = ov[m][bj]; const f32x2 oa = __builtin_amdgcn_cvt_pk_f32_fp8((int)o.x, false), ob = __builtin_amdgcn_cvt_pk_f32_fp8((int)o.x, true), oc = __builtin_amdgcn_cvt_pk_f32_fp8((int)o.y, false), od = __builtin_amdgcn_cvt_pk_f32_fp8((int)o.y, true);
;                         v0[0] += oa[0]; v0[1] += oa[1]; v0[2] += ob[0]; v0[3] += ob[1]; v1[0] += oc[0]; v1[1] += oc[1]; v1[2] += od[0]; v1[3] += od[1];
;                     }
;                     o8v[bj].x = pk4_fp8(v0[0], v0[1], v0[2], v0[3]); o8v[bj].y = pk4_fp8(v1[0], v1[1], v1[2], v1[3]); }
;                 st_pair16((ADD ? mix8 : (unsigned char*)mix) + r * 1024 + col0, 128, o8v[0], o8v[1], fq); }
	v_cvt_pk_f32_fp8_e32 v[94:95], v86
	v_cvt_pk_f32_fp8_sdwa v[96:97], v86 src0_sel:WORD_1
	v_cvt_pk_f32_fp8_e32 v[98:99], v87
	v_cvt_pk_f32_fp8_sdwa v[86:87], v87 src0_sel:WORD_1
	v_fma_f32 v74, v74, v100, v94
	v_fmac_f32_e32 v95, v75, v101
	v_fma_f32 v75, v76, v102, v96
	v_fma_f32 v76, v70, v104, v98
	v_fmac_f32_e32 v99, v71, v105
	v_fmac_f32_e32 v87, v73, v107
	v_med3_f32 v71, v74, s35, v225
	v_med3_f32 v73, v95, s35, v225
	v_mov_b32_e32 v70, v4
	v_cvt_pk_fp8_f32 v70, v71, v73
	v_med3_f32 v73, v75, s35, v225
	v_med3_f32 v75, v76, s35, v225
	v_med3_f32 v76, v99, s35, v225
	v_mov_b32_e32 v71, v4
	v_cvt_pk_fp8_f32 v71, v75, v76
	v_fmac_f32_e32 v97, v77, v103
	v_fma_f32 v72, v72, v106, v86
	v_med3_f32 v74, v97, s35, v225
	v_cvt_pk_fp8_f32 v70, v73, v74 op_sel:[0,0,1]
	v_med3_f32 v72, v72, s35, v225
	v_med3_f32 v73, v87, s35, v225
	v_cvt_pk_fp8_f32 v71, v72, v73 op_sel:[0,0,1]
	v_cvt_f32_ubyte0_e32 v72, v160
	v_mul_f32_e32 v86, 0x38808081, v72
	v_cvt_f32_ubyte1_e32 v72, v160
	v_mul_f32_e32 v87, 0x38808081, v72
	v_cvt_f32_ubyte2_e32 v72, v160
	v_mul_f32_e32 v94, 0x38808081, v72
	v_cvt_f32_ubyte3_e32 v72, v160
	v_mul_f32_e32 v95, 0x38808081, v72
	v_cvt_f32_ubyte0_e32 v72, v161
	v_mul_f32_e32 v96, 0x38808081, v72
	v_cvt_f32_ubyte1_e32 v72, v161
	v_mul_f32_e32 v97, 0x38808081, v72
	v_cvt_f32_ubyte2_e32 v72, v161
	v_mul_f32_e32 v98, 0x38808081, v72
	v_cvt_f32_ubyte3_e32 v72, v161
	v_mul_f32_e32 v99, 0x38808081, v72
	s_waitcnt vmcnt(7)
	v_cvt_pk_f32_fp8_e32 v[72:73], v84
	v_cvt_pk_f32_fp8_e32 v[76:77], v85
	v_cvt_pk_f32_fp8_sdwa v[74:75], v84 src0_sel:WORD_1
	v_cvt_pk_f32_fp8_sdwa v[84:85], v85 src0_sel:WORD_1
	v_fma_f32 v58, v58, v86, v72
	v_fmac_f32_e32 v73, v59, v87
	v_fma_f32 v54, v54, v96, v76
	v_fmac_f32_e32 v77, v55, v97
	v_fma_f32 v55, v56, v98, v84
	v_fmac_f32_e32 v85, v57, v99
	v_med3_f32 v56, v58, s35, v225
	v_med3_f32 v57, v73, s35, v225
	v_mov_b32_e32 v72, v4
	v_med3_f32 v54, v54, s35, v225
	v_med3_f32 v58, v77, s35, v225
	v_mov_b32_e32 v73, v4
	v_cvt_pk_fp8_f32 v72, v56, v57
	v_cvt_pk_fp8_f32 v73, v54, v58
	v_fma_f32 v59, v60, v94, v74
	v_fmac_f32_e32 v75, v61, v95
	v_med3_f32 v56, v59, s35, v225
	v_med3_f32 v57, v75, s35, v225
	v_med3_f32 v54, v55, s35, v225
	v_med3_f32 v55, v85, s35, v225
	v_cvt_pk_fp8_f32 v72, v56, v57 op_sel:[0,0,1]
	v_cvt_pk_fp8_f32 v73, v54, v55 op_sel:[0,0,1]
	v_lshl_add_u64 v[54:55], s[44:45], 0, v[82:83]
	v_lshl_add_u64 v[54:55], v[54:55], 0, v[144:145]
	v_permlane16_swap_b32_e32 v70, v72
	v_permlane16_swap_b32_e32 v71, v73
	v_lshl_add_u64 v[54:55], v[54:55], 0, v[146:147]
	global_store_dwordx4 v[54:55], v[70:73], off
	v_cvt_f32_ubyte0_e32 v54, v158
	s_waitcnt vmcnt(6)
	v_cvt_pk_f32_fp8_sdwa v[56:57], v90 src0_sel:WORD_1
	v_mul_f32_e32 v70, 0x38808081, v54
	v_cvt_f32_ubyte1_e32 v54, v158
	v_mul_f32_e32 v71, 0x38808081, v54
	v_cvt_f32_ubyte2_e32 v54, v158
	v_mul_f32_e32 v72, 0x38808081, v54
	v_cvt_f32_ubyte3_e32 v54, v158
	v_mul_f32_e32 v73, 0x38808081, v54
	v_cvt_f32_ubyte0_e32 v54, v159
	v_mul_f32_e32 v74, 0x38808081, v54
	v_cvt_f32_ubyte1_e32 v54, v159
	v_mul_f32_e32 v75, 0x38808081, v54
	v_cvt_f32_ubyte2_e32 v54, v159
	v_mul_f32_e32 v76, 0x38808081, v54
	v_cvt_f32_ubyte3_e32 v54, v159
	v_mul_f32_e32 v77, 0x38808081, v54
	v_cvt_pk_f32_fp8_e32 v[54:55], v90
	v_cvt_pk_f32_fp8_e32 v[58:59], v91
	v_cvt_pk_f32_fp8_sdwa v[60:61], v91 src0_sel:WORD_1
	v_fmac_f32_e32 v57, v53, v73
	v_fma_f32 v50, v50, v70, v54
	v_fmac_f32_e32 v55, v51, v71
	v_fma_f32 v51, v52, v72, v56
	v_fma_f32 v52, v46, v74, v58
	v_fmac_f32_e32 v59, v47, v75
	v_fmac_f32_e32 v61, v49, v77
	v_med3_f32 v47, v50, s35, v225
	v_med3_f32 v49, v55, s35, v225
	v_mov_b32_e32 v46, v4
	v_cvt_pk_fp8_f32 v46, v47, v49
	v_med3_f32 v49, v51, s35, v225
	v_med3_f32 v51, v52, s35, v225
	v_med3_f32 v52, v59, s35, v225
	v_mov_b32_e32 v47, v4
	v_cvt_pk_fp8_f32 v47, v51, v52
	v_fma_f32 v48, v48, v76, v60
	v_med3_f32 v50, v57, s35, v225
	v_cvt_pk_fp8_f32 v46, v49, v50 op_sel:[0,0,1]
	v_med3_f32 v48, v48, s35, v225
	v_med3_f32 v49, v61, s35, v225
	v_cvt_pk_fp8_f32 v47, v48, v49 op_sel:[0,0,1]
	v_cvt_f32_ubyte0_e32 v48, v156
	v_mul_f32_e32 v56, 0x38808081, v48
	v_cvt_f32_ubyte1_e32 v48, v156
	v_mul_f32_e32 v57, 0x38808081, v48
	v_cvt_f32_ubyte2_e32 v48, v156
	v_mul_f32_e32 v58, 0x38808081, v48
	v_cvt_f32_ubyte3_e32 v48, v156
	v_mul_f32_e32 v59, 0x38808081, v48
	v_cvt_f32_ubyte0_e32 v48, v157
	v_mul_f32_e32 v60, 0x38808081, v48
	v_cvt_f32_ubyte1_e32 v48, v157
	v_mul_f32_e32 v61, 0x38808081, v48
	v_cvt_f32_ubyte2_e32 v48, v157
	v_mul_f32_e32 v70, 0x38808081, v48
	v_cvt_f32_ubyte3_e32 v48, v157
	v_mul_f32_e32 v71, 0x38808081, v48
	s_waitcnt vmcnt(5)
	v_cvt_pk_f32_fp8_e32 v[48:49], v92
	v_cvt_pk_f32_fp8_e32 v[52:53], v93
	v_cvt_pk_f32_fp8_sdwa v[54:55], v93 src0_sel:WORD_1
	v_cvt_pk_f32_fp8_sdwa v[50:51], v92 src0_sel:WORD_1
	v_fma_f32 v42, v42, v56, v48
	v_fmac_f32_e32 v49, v43, v57
	v_fma_f32 v38, v38, v60, v52
	v_fmac_f32_e32 v53, v39, v61
	v_fma_f32 v39, v40, v70, v54
	v_fmac_f32_e32 v55, v41, v71
	v_med3_f32 v40, v42, s35, v225
	v_med3_f32 v41, v49, s35, v225
	v_mov_b32_e32 v48, v4
	v_med3_f32 v38, v38, s35, v225
	v_med3_f32 v42, v53, s35, v225
	v_mov_b32_e32 v49, v4
	v_cvt_pk_fp8_f32 v48, v40, v41
	v_cvt_pk_fp8_f32 v49, v38, v42
	v_fma_f32 v43, v44, v58, v50
	v_fmac_f32_e32 v51, v45, v59
	v_med3_f32 v40, v43, s35, v225
	v_med3_f32 v41, v51, s35, v225
	v_med3_f32 v38, v39, s35, v225
	v_med3_f32 v39, v55, s35, v225
	v_cvt_pk_fp8_f32 v48, v40, v41 op_sel:[0,0,1]
	v_cvt_pk_fp8_f32 v49, v38, v39 op_sel:[0,0,1]
	v_lshl_add_u64 v[38:39], s[44:45], 0, v[88:89]
	v_lshl_add_u64 v[38:39], v[38:39], 0, v[144:145]
	v_permlane16_swap_b32_e32 v46, v48
	v_permlane16_swap_b32_e32 v47, v49
	v_lshl_add_u64 v[38:39], v[38:39], 0, v[146:147]
	global_store_dwordx4 v[38:39], v[46:49], off
	v_cvt_f32_ubyte0_e32 v38, v154
	s_waitcnt vmcnt(5)
; DI unsigned pk4_fp8(float a, float b, float c_, float d) { int w = 0; w = __builtin_amdgcn_cvt_pk_fp8_f32(clamp8(a), clamp8(b), w, false); w = __builtin_amdgcn_cvt_pk_fp8_f32(clamp8(c_), clamp8(d), w, true); return (unsigned)w; }
; #define PG8_BAR __builtin_amdgcn_s_barrier()
; template <class Epi, class Sched, bool F8 = false>
; DI void gemm_phase(LAS unsigned char* lds, const int K, const Sched& S, const Epi& E) {
;     ...
;         if (!has_next) break;
;         if constexpr (!F8)
; #pragma unroll
;         for (int a = 0; a < 2; ++a)
; #pragma unroll
;             for (int b = 0; b < 2; ++b)
; #pragma unroll
;                 for (int m = 0; m < 4; ++m)
; #pragma unroll
;                     for (int n = 0; n < 2; ++n) acc[a][b][m][n] = (f32x4){0.f, 0.f, 0.f, 0.f};
;         cur = nxt; cA = nA; cB = nB; ++ui;
;         if (wr == 1) PG8_BAR;
;     DI void operator()(const f32x4 (&acc)[2][2][4][2], const Unit& u, int wr, int wc, int fr, int fq) const {
;     ...
;             for (int m = 0; m < 4; ++m) { const size_t r = (size_t)(row0 + ai * 128 + m * 16); u32x2 o8v[2];
; #pragma unroll
;                 for (int bj = 0; bj < 2; ++bj) {
;                     const u32x2 gg = g[ai][m][bj];
;                     f32x4 v0 = acc[ai][bj][m][0], v1 = acc[ai][bj][m][1];
;                     v0[0] *= (float)((gg.x >> 0) & 0xffu) * k; v0[1] *= (float)((gg.x >> 8) & 0xffu) * k; v0[2] *= (float)((gg.x >> 16) & 0xffu) * k; v0[3] *= (float)((gg.x >> 24) & 0xffu) * k;
;                     v1[0] *= (float)((gg.y >> 0) & 0xffu) * k; v1[1] *= (float)((gg.y >> 8) & 0xffu) * k; v1[2] *= (float)((gg.y >> 16) & 0xffu) * k; v1[3] *= (float)((gg.y >> 24) & 0xffu) * k;
;                     if (ADD) { const u32x2 o = ov[m][bj]; const f32x2 oa = __builtin_amdgcn_cvt_pk_f32_fp8((int)o.x, false), ob = __builtin_amdgcn_cvt_pk_f32_fp8((int)o.x, true), oc = __builtin_amdgcn_cvt_pk_f32_fp8((int)o.y, false), od = __builtin_amdgcn_cvt_pk_f32_fp8((int)o.y, true);
;                         v0[0] += oa[0]; v0[1] += oa[1]; v0[2] += ob[0]; v0[3] += ob[1]; v1[0] += oc[0]; v1[1] += oc[1]; v1[2] += od[0]; v1[3] += od[1];
;                     }
;                     o8v[bj].x = pk4_fp8(v0[0], v0[1], v0[2], v0[3]); o8v[bj].y = pk4_fp8(v1[0], v1[1], v1[2], v1[3]); }
;                 st_pair16((ADD ? mix8 : (unsigned char*)mix) + r * 1024 + col0, 128, o8v[0], o8v[1], fq); }
	v_cvt_pk_f32_fp8_sdwa v[40:41], v80 src0_sel:WORD_1
	v_mul_f32_e32 v46, 0x38808081, v38
	v_cvt_f32_ubyte1_e32 v38, v154
	v_mul_f32_e32 v47, 0x38808081, v38
	v_cvt_f32_ubyte2_e32 v38, v154
	v_mul_f32_e32 v48, 0x38808081, v38
	v_cvt_f32_ubyte3_e32 v38, v154
	v_mul_f32_e32 v49, 0x38808081, v38
	v_cvt_f32_ubyte0_e32 v38, v155
	v_mul_f32_e32 v50, 0x38808081, v38
	v_cvt_f32_ubyte1_e32 v38, v155
	v_mul_f32_e32 v51, 0x38808081, v38
	v_cvt_f32_ubyte2_e32 v38, v155
	v_mul_f32_e32 v52, 0x38808081, v38
	v_cvt_f32_ubyte3_e32 v38, v155
	v_mul_f32_e32 v53, 0x38808081, v38
	v_cvt_pk_f32_fp8_e32 v[38:39], v80
	v_cvt_pk_f32_fp8_e32 v[42:43], v81
	v_cvt_pk_f32_fp8_sdwa v[44:45], v81 src0_sel:WORD_1
	v_fmac_f32_e32 v41, v37, v49
	v_fma_f32 v34, v34, v46, v38
	v_fmac_f32_e32 v39, v35, v47
	v_fma_f32 v35, v36, v48, v40
	v_fma_f32 v36, v30, v50, v42
	v_fmac_f32_e32 v43, v31, v51
	v_fmac_f32_e32 v45, v33, v53
	v_med3_f32 v31, v34, s35, v225
	v_med3_f32 v33, v39, s35, v225
	v_mov_b32_e32 v30, v4
	v_cvt_pk_fp8_f32 v30, v31, v33
	v_med3_f32 v33, v35, s35, v225
	v_med3_f32 v35, v36, s35, v225
	v_med3_f32 v36, v43, s35, v225
	v_mov_b32_e32 v31, v4
	v_cvt_pk_fp8_f32 v31, v35, v36
	v_fma_f32 v32, v32, v52, v44
	v_med3_f32 v34, v41, s35, v225
	v_cvt_pk_fp8_f32 v30, v33, v34 op_sel:[0,0,1]
	v_med3_f32 v32, v32, s35, v225
	v_med3_f32 v33, v45, s35, v225
	v_cvt_pk_fp8_f32 v31, v32, v33 op_sel:[0,0,1]
	v_cvt_f32_ubyte0_e32 v32, v152
	v_mul_f32_e32 v40, 0x38808081, v32
	v_cvt_f32_ubyte1_e32 v32, v152
	v_mul_f32_e32 v41, 0x38808081, v32
	v_cvt_f32_ubyte2_e32 v32, v152
	v_mul_f32_e32 v42, 0x38808081, v32
	v_cvt_f32_ubyte3_e32 v32, v152
	v_mul_f32_e32 v43, 0x38808081, v32
	v_cvt_f32_ubyte0_e32 v32, v153
	v_mul_f32_e32 v44, 0x38808081, v32
	v_cvt_f32_ubyte1_e32 v32, v153
	v_mul_f32_e32 v45, 0x38808081, v32
	v_cvt_f32_ubyte2_e32 v32, v153
	v_mul_f32_e32 v46, 0x38808081, v32
	v_cvt_f32_ubyte3_e32 v32, v153
	v_mul_f32_e32 v47, 0x38808081, v32
	s_waitcnt vmcnt(4)
	v_cvt_pk_f32_fp8_e32 v[32:33], v78
	v_cvt_pk_f32_fp8_e32 v[36:37], v79
	v_cvt_pk_f32_fp8_sdwa v[38:39], v79 src0_sel:WORD_1
	v_cvt_pk_f32_fp8_sdwa v[34:35], v78 src0_sel:WORD_1
	v_fma_f32 v26, v26, v40, v32
	v_fmac_f32_e32 v33, v27, v41
	v_fma_f32 v22, v22, v44, v36
	v_fmac_f32_e32 v37, v23, v45
	v_fma_f32 v23, v24, v46, v38
	v_fmac_f32_e32 v39, v25, v47
	v_med3_f32 v24, v26, s35, v225
	v_med3_f32 v25, v33, s35, v225
	v_mov_b32_e32 v32, v4
	v_med3_f32 v22, v22, s35, v225
	v_med3_f32 v26, v37, s35, v225
	v_mov_b32_e32 v33, v4
	v_cvt_pk_fp8_f32 v32, v24, v25
	v_cvt_pk_fp8_f32 v33, v22, v26
	v_fma_f32 v27, v28, v42, v34
	v_fmac_f32_e32 v35, v29, v43
	v_med3_f32 v24, v27, s35, v225
	v_med3_f32 v25, v35, s35, v225
	v_med3_f32 v22, v23, s35, v225
	v_med3_f32 v23, v39, s35, v225
	v_cvt_pk_fp8_f32 v32, v24, v25 op_sel:[0,0,1]
	v_cvt_pk_fp8_f32 v33, v22, v23 op_sel:[0,0,1]
	v_lshl_add_u64 v[22:23], s[44:45], 0, v[68:69]
	v_lshl_add_u64 v[22:23], v[22:23], 0, v[144:145]
	v_permlane16_swap_b32_e32 v30, v32
	v_permlane16_swap_b32_e32 v31, v33
	v_lshl_add_u64 v[22:23], v[22:23], 0, v[146:147]
	global_store_dwordx4 v[22:23], v[30:33], off
	v_cvt_f32_ubyte0_e32 v22, v150
	s_waitcnt vmcnt(4)
	v_cvt_pk_f32_fp8_sdwa v[24:25], v66 src0_sel:WORD_1
	v_mul_f32_e32 v30, 0x38808081, v22
	v_cvt_f32_ubyte1_e32 v22, v150
	v_mul_f32_e32 v31, 0x38808081, v22
	v_cvt_f32_ubyte2_e32 v22, v150
	v_mul_f32_e32 v32, 0x38808081, v22
	v_cvt_f32_ubyte3_e32 v22, v150
	v_mul_f32_e32 v33, 0x38808081, v22
	v_cvt_f32_ubyte0_e32 v22, v151
	v_mul_f32_e32 v34, 0x38808081, v22
	v_cvt_f32_ubyte1_e32 v22, v151
	v_mul_f32_e32 v35, 0x38808081, v22
	v_cvt_f32_ubyte2_e32 v22, v151
	v_mul_f32_e32 v36, 0x38808081, v22
	v_cvt_f32_ubyte3_e32 v22, v151
	v_mul_f32_e32 v37, 0x38808081, v22
	v_cvt_pk_f32_fp8_e32 v[22:23], v66
	v_cvt_pk_f32_fp8_e32 v[26:27], v67
	v_cvt_pk_f32_fp8_sdwa v[28:29], v67 src0_sel:WORD_1
	v_fmac_f32_e32 v25, v21, v33
	v_fma_f32 v18, v18, v30, v22
	v_fmac_f32_e32 v23, v19, v31
	v_fma_f32 v19, v20, v32, v24
	v_fma_f32 v20, v14, v34, v26
	v_fmac_f32_e32 v27, v15, v35
	v_fmac_f32_e32 v29, v17, v37
	v_med3_f32 v15, v18, s35, v225
	v_med3_f32 v17, v23, s35, v225
	v_mov_b32_e32 v14, v4
	v_cvt_pk_fp8_f32 v14, v15, v17
	v_med3_f32 v17, v19, s35, v225
	v_med3_f32 v19, v20, s35, v225
	v_med3_f32 v20, v27, s35, v225
	v_mov_b32_e32 v15, v4
	v_cvt_pk_fp8_f32 v15, v19, v20
	v_fma_f32 v16, v16, v36, v28
	v_med3_f32 v18, v25, s35, v225
	v_cvt_pk_fp8_f32 v14, v17, v18 op_sel:[0,0,1]
	v_med3_f32 v16, v16, s35, v225
	v_med3_f32 v17, v29, s35, v225
	v_cvt_pk_fp8_f32 v15, v16, v17 op_sel:[0,0,1]
	v_cvt_f32_ubyte0_e32 v16, v148
	v_mul_f32_e32 v24, 0x38808081, v16
	v_cvt_f32_ubyte1_e32 v16, v148
	v_mul_f32_e32 v25, 0x38808081, v16
	v_cvt_f32_ubyte2_e32 v16, v148
	v_mul_f32_e32 v26, 0x38808081, v16
	v_cvt_f32_ubyte3_e32 v16, v148
	v_mul_f32_e32 v27, 0x38808081, v16
	v_cvt_f32_ubyte0_e32 v16, v149
	v_mul_f32_e32 v28, 0x38808081, v16
	v_cvt_f32_ubyte1_e32 v16, v149
	v_mul_f32_e32 v29, 0x38808081, v16
	v_cvt_f32_ubyte2_e32 v16, v149
	v_mul_f32_e32 v30, 0x38808081, v16
	v_cvt_f32_ubyte3_e32 v16, v149
	v_mul_f32_e32 v31, 0x38808081, v16
	s_waitcnt vmcnt(3)
	v_cvt_pk_f32_fp8_e32 v[16:17], v64
	v_cvt_pk_f32_fp8_e32 v[20:21], v65
	v_cvt_pk_f32_fp8_sdwa v[22:23], v65 src0_sel:WORD_1
	v_cvt_pk_f32_fp8_sdwa v[18:19], v64 src0_sel:WORD_1
	v_fma_f32 v10, v10, v24, v16
	v_fmac_f32_e32 v17, v11, v25
	v_fma_f32 v6, v6, v28, v20
	v_fmac_f32_e32 v21, v7, v29
	v_fma_f32 v7, v8, v30, v22
	v_fmac_f32_e32 v23, v9, v31
	v_med3_f32 v8, v10, s35, v225
	v_med3_f32 v9, v17, s35, v225
	v_mov_b32_e32 v16, v4
	v_med3_f32 v6, v6, s35, v225
	v_med3_f32 v10, v21, s35, v225
	v_mov_b32_e32 v17, v4
	v_cvt_pk_fp8_f32 v16, v8, v9
	v_cvt_pk_fp8_f32 v17, v6, v10
	v_fma_f32 v11, v12, v26, v18
	v_fmac_f32_e32 v19, v13, v27
	v_med3_f32 v8, v11, s35, v225
	v_med3_f32 v9, v19, s35, v225
	v_med3_f32 v6, v7, s35, v225
	v_med3_f32 v7, v23, s35, v225
	v_cvt_pk_fp8_f32 v16, v8, v9 op_sel:[0,0,1]
	v_cvt_pk_fp8_f32 v17, v6, v7 op_sel:[0,0,1]
	v_lshl_add_u64 v[6:7], s[44:45], 0, v[62:63]
	v_lshl_add_u64 v[6:7], v[6:7], 0, v[144:145]
	v_permlane16_swap_b32_e32 v14, v16
	v_permlane16_swap_b32_e32 v15, v17
	v_lshl_add_u64 v[6:7], v[6:7], 0, v[146:147]
	global_store_dwordx4 v[6:7], v[14:17], off
	s_cbranch_vccnz .LBB0_966
	s_andn2_b64 vcc, exec, s[16:17]
	s_cbranch_vccnz .LBB0_965
	s_barrier
	s_branch .LBB0_965

; #define GAS __attribute__((address_space(1)))
; DI u32x4 pack8(const f32x4& v0, const f32x4& v1) { u32x4 w; w.x = cvt_pk_bf16(v0[0], v0[1]); w.y = cvt_pk_bf16(v0[2], v0[3]); w.z = cvt_pk_bf16(v1[0], v1[1]); w.w = cvt_pk_bf16(v1[2], v1[3]); return w; }
;     DI void operator()(const f32x4 (&acc)[2][2][4][2], const Unit& u, int wr, int wc, int fr, int fq) const {
;         asm volatile("" : "+v"(fr), "+v"(fq));
;         const int row0 = u.pm * 256 + wr * 64 + fr, col0 = u.pn * 256 + wc * 32 + 8 * fq;
;         if (x32) {
; #pragma unroll
;             for (int ai = 0; ai < 2; ++ai)
; #pragma unroll
;                 for (int m2 = 0; m2 < 4; m2 += 2) { f32x4 a[2][2][2];
; #pragma unroll
;                     for (int mm = 0; mm < 2; ++mm)
; #pragma unroll
;                         for (int bj = 0; bj < 2; ++bj) { const size_t off = (size_t)(row0 + ai * 128 + (m2 + mm) * 16) * 1024 + col0 + bj * 128; a[mm][bj][0] = *(const GAS f32x4*)(x32 + off); a[mm][bj][1] = *(const GAS f32x4*)(x32 + off + 4); }
;                     asm volatile("" ::: "memory");
; #pragma unroll
;                     for (int mm = 0; mm < 2; ++mm)
; #pragma unroll
;                         for (int bj = 0; bj < 2; ++bj) { const size_t off = (size_t)(row0 + ai * 128 + (m2 + mm) * 16) * 1024 + col0 + bj * 128;
;                             *(GAS u32x4*)(xr + off) = pack8(a[mm][bj][0] * DN_ALPHA + acc[ai][bj][m2 + mm][0] * W8_INV, a[mm][bj][1] * DN_ALPHA + acc[ai][bj][m2 + mm][1] * W8_INV); }
.LBB0_1046:
	s_lshl_b32 s7, s16, 8
	v_mov_b32_e32 v6, v1
	v_mov_b32_e32 v7, v5
	s_add_i32 s7, s7, s87
	s_lshl_b32 s5, s5, 8
	s_nop 15
	s_or_b32 s5, s5, s88
	v_add_u32_e32 v10, s7, v6
	v_lshl_add_u32 v6, v7, 3, s5
	v_ashrrev_i32_e32 v11, 31, v10
	v_ashrrev_i32_e32 v7, 31, v6
	v_lshlrev_b64 v[28:29], 11, v[10:11]
	s_andn2_b64 vcc, exec, s[48:49]
	v_lshlrev_b64 v[26:27], 1, v[6:7]
	v_lshl_add_u64 v[30:31], s[44:45], 0, v[28:29]
	s_cbranch_vccnz .LBB0_1052
	v_lshl_add_u64 v[12:13], v[6:7], 2, s[42:43]
	v_lshlrev_b64 v[6:7], 12, v[10:11]
	v_lshl_add_u64 v[22:23], v[12:13], 0, v[6:7]
	global_load_dwordx4 v[6:9], v[22:23], off offset:16
	global_load_dwordx4 v[14:17], v[22:23], off
	global_load_dwordx4 v[18:21], v[22:23], off offset:528
	s_nop 0
	global_load_dwordx4 v[22:25], v[22:23], off offset:512
	v_add_u32_e32 v36, 16, v10
	v_ashrrev_i32_e32 v37, 31, v36
	v_lshlrev_b64 v[32:33], 12, v[36:37]
	v_lshl_add_u64 v[190:191], v[12:13], 0, v[32:33]
	global_load_dwordx4 v[32:35], v[190:191], off offset:16
	global_load_dwordx4 v[180:183], v[190:191], off
	global_load_dwordx4 v[184:187], v[190:191], off offset:528
	s_nop 0
	global_load_dwordx4 v[190:193], v[190:191], off offset:512
	s_waitcnt vmcnt(0)
	v_pk_mul_f32 v[8:9], v[8:9], s[12:13] op_sel_hi:[1,0]
	v_pk_mul_f32 v[16:17], v[16:17], s[12:13] op_sel_hi:[1,0]
	v_pk_mul_f32 v[14:15], v[14:15], s[12:13] op_sel_hi:[1,0]
	v_pk_mul_f32 v[6:7], v[6:7], s[12:13] op_sel_hi:[1,0]
	v_pk_fma_f32 v[16:17], v[164:165], s[34:35], v[16:17] op_sel_hi:[1,0,1]
	v_pk_fma_f32 v[14:15], v[162:163], s[34:35], v[14:15] op_sel_hi:[1,0,1]
	v_pk_fma_f32 v[194:195], v[160:161], s[34:35], v[8:9] op_sel_hi:[1,0,1]
	v_pk_fma_f32 v[8:9], v[158:159], s[34:35], v[6:7] op_sel_hi:[1,0,1]
	v_cvt_pk_bf16_f32 v6, v14, v15
	v_cvt_pk_bf16_f32 v7, v16, v17
	v_cvt_pk_bf16_f32 v8, v8, v9
	v_cvt_pk_bf16_f32 v9, v194, v195
	v_lshl_add_u64 v[14:15], v[30:31], 0, v[26:27]
	global_store_dwordx4 v[14:15], v[6:9], off
	v_pk_mul_f32 v[18:19], v[18:19], s[12:13] op_sel_hi:[1,0]
	s_nop 0
	v_pk_mul_f32 v[6:7], v[24:25], s[12:13] op_sel_hi:[1,0]
	v_pk_mul_f32 v[8:9], v[22:23], s[12:13] op_sel_hi:[1,0]
	v_pk_fma_f32 v[16:17], v[156:157], s[34:35], v[6:7] op_sel_hi:[1,0,1]
	v_pk_fma_f32 v[6:7], v[154:155], s[34:35], v[8:9] op_sel_hi:[1,0,1]
	v_pk_mul_f32 v[8:9], v[20:21], s[12:13] op_sel_hi:[1,0]
	v_cvt_pk_bf16_f32 v6, v6, v7
	v_pk_fma_f32 v[20:21], v[152:153], s[34:35], v[8:9] op_sel_hi:[1,0,1]
	v_pk_fma_f32 v[8:9], v[150:151], s[34:35], v[18:19] op_sel_hi:[1,0,1]
	v_cvt_pk_bf16_f32 v7, v16, v17
	v_cvt_pk_bf16_f32 v8, v8, v9
	v_cvt_pk_bf16_f32 v9, v20, v21
	global_store_dwordx4 v[14:15], v[6:9], off offset:256
	v_lshlrev_b64 v[14:15], 11, v[36:37]
	v_pk_mul_f32 v[18:19], v[32:33], s[12:13] op_sel_hi:[1,0]
	v_pk_mul_f32 v[6:7], v[182:183], s[12:13] op_sel_hi:[1,0]
	v_pk_mul_f32 v[8:9], v[180:181], s[12:13] op_sel_hi:[1,0]
	v_pk_fma_f32 v[16:17], v[148:149], s[34:35], v[6:7] op_sel_hi:[1,0,1]
	v_pk_fma_f32 v[6:7], v[146:147], s[34:35], v[8:9] op_sel_hi:[1,0,1]
	v_pk_mul_f32 v[8:9], v[34:35], s[12:13] op_sel_hi:[1,0]
	v_lshl_add_u64 v[14:15], s[44:45], 0, v[14:15]
	v_pk_fma_f32 v[20:21], v[144:145], s[34:35], v[8:9] op_sel_hi:[1,0,1]
	v_pk_fma_f32 v[8:9], v[142:143], s[34:35], v[18:19] op_sel_hi:[1,0,1]
	v_cvt_pk_bf16_f32 v6, v6, v7
	v_cvt_pk_bf16_f32 v7, v16, v17
	v_cvt_pk_bf16_f32 v8, v8, v9
	v_cvt_pk_bf16_f32 v9, v20, v21
	v_lshl_add_u64 v[14:15], v[14:15], 0, v[26:27]
	global_store_dwordx4 v[14:15], v[6:9], off
	v_pk_mul_f32 v[18:19], v[184:185], s[12:13] op_sel_hi:[1,0]
	s_nop 0
	v_pk_mul_f32 v[6:7], v[192:193], s[12:13] op_sel_hi:[1,0]
	v_pk_mul_f32 v[8:9], v[190:191], s[12:13] op_sel_hi:[1,0]
	v_pk_fma_f32 v[16:17], v[140:141], s[34:35], v[6:7] op_sel_hi:[1,0,1]
	v_pk_fma_f32 v[6:7], v[138:139], s[34:35], v[8:9] op_sel_hi:[1,0,1]
	v_pk_mul_f32 v[8:9], v[186:187], s[12:13] op_sel_hi:[1,0]
	v_cvt_pk_bf16_f32 v6, v6, v7
	v_pk_fma_f32 v[20:21], v[136:137], s[34:35], v[8:9] op_sel_hi:[1,0,1]
	v_pk_fma_f32 v[8:9], v[134:135], s[34:35], v[18:19] op_sel_hi:[1,0,1]
	v_cvt_pk_bf16_f32 v7, v16, v17
	v_cvt_pk_bf16_f32 v8, v8, v9
	v_cvt_pk_bf16_f32 v9, v20, v21
	global_store_dwordx4 v[14:15], v[6:9], off offset:256
	v_add_u32_e32 v14, 32, v10
	v_ashrrev_i32_e32 v15, 31, v14
	v_lshlrev_b64 v[6:7], 12, v[14:15]
	v_lshl_add_u64 v[24:25], v[12:13], 0, v[6:7]
	global_load_dwordx4 v[6:9], v[24:25], off offset:16
	global_load_dwordx4 v[16:19], v[24:25], off
	global_load_dwordx4 v[20:23], v[24:25], off offset:528
	global_load_dwordx4 v[32:35], v[24:25], off offset:512
	v_add_u32_e32 v24, 48, v10
	v_ashrrev_i32_e32 v25, 31, v24
	v_lshlrev_b64 v[36:37], 12, v[24:25]
	v_lshl_add_u64 v[36:37], v[12:13], 0, v[36:37]
	global_load_dwordx4 v[180:183], v[36:37], off offset:16
	global_load_dwordx4 v[184:187], v[36:37], off
	global_load_dwordx4 v[190:193], v[36:37], off offset:528
	global_load_dwordx4 v[194:197], v[36:37], off offset:512
	v_lshlrev_b64 v[14:15], 11, v[14:15]
	v_lshl_add_u64 v[14:15], s[44:45], 0, v[14:15]
	v_lshl_add_u64 v[14:15], v[14:15], 0, v[26:27]
	s_waitcnt vmcnt(7)
	v_pk_mul_f32 v[8:9], v[8:9], s[12:13] op_sel_hi:[1,0]
	s_waitcnt vmcnt(6)
	v_pk_mul_f32 v[18:19], v[18:19], s[12:13] op_sel_hi:[1,0]
	v_pk_mul_f32 v[16:17], v[16:17], s[12:13] op_sel_hi:[1,0]
	v_pk_mul_f32 v[6:7], v[6:7], s[12:13] op_sel_hi:[1,0]
	v_pk_fma_f32 v[18:19], v[132:133], s[34:35], v[18:19] op_sel_hi:[1,0,1]
	v_pk_fma_f32 v[16:17], v[130:131], s[34:35], v[16:17] op_sel_hi:[1,0,1]
	v_pk_fma_f32 v[36:37], v[128:129], s[34:35], v[8:9] op_sel_hi:[1,0,1]
	v_pk_fma_f32 v[8:9], v[126:127], s[34:35], v[6:7] op_sel_hi:[1,0,1]
	v_cvt_pk_bf16_f32 v6, v16, v17
	v_cvt_pk_bf16_f32 v7, v18, v19
	v_cvt_pk_bf16_f32 v8, v8, v9
	v_cvt_pk_bf16_f32 v9, v36, v37
	global_store_dwordx4 v[14:15], v[6:9], off
	s_waitcnt vmcnt(6)
; #define GAS __attribute__((address_space(1)))
; DI u32x4 pack8(const f32x4& v0, const f32x4& v1) { u32x4 w; w.x = cvt_pk_bf16(v0[0], v0[1]); w.y = cvt_pk_bf16(v0[2], v0[3]); w.z = cvt_pk_bf16(v1[0], v1[1]); w.w = cvt_pk_bf16(v1[2], v1[3]); return w; }
;     DI void operator()(const f32x4 (&acc)[2][2][4][2], const Unit& u, int wr, int wc, int fr, int fq) const {
;     ...
;                 for (int m2 = 0; m2 < 4; m2 += 2) { f32x4 a[2][2][2];
; #pragma unroll
;                     for (int mm = 0; mm < 2; ++mm)
; #pragma unroll
;                         for (int bj = 0; bj < 2; ++bj) { const size_t off = (size_t)(row0 + ai * 128 + (m2 + mm) * 16) * 1024 + col0 + bj * 128; a[mm][bj][0] = *(const GAS f32x4*)(x32 + off); a[mm][bj][1] = *(const GAS f32x4*)(x32 + off + 4); }
;                     asm volatile("" ::: "memory");
; #pragma unroll
;                     for (int mm = 0; mm < 2; ++mm)
; #pragma unroll
;                         for (int bj = 0; bj < 2; ++bj) { const size_t off = (size_t)(row0 + ai * 128 + (m2 + mm) * 16) * 1024 + col0 + bj * 128;
;                             *(GAS u32x4*)(xr + off) = pack8(a[mm][bj][0] * DN_ALPHA + acc[ai][bj][m2 + mm][0] * W8_INV, a[mm][bj][1] * DN_ALPHA + acc[ai][bj][m2 + mm][1] * W8_INV); }
;                     asm volatile("" ::: "memory"); }
	v_pk_mul_f32 v[18:19], v[20:21], s[12:13] op_sel_hi:[1,0]
	s_waitcnt vmcnt(5)
	v_pk_mul_f32 v[6:7], v[34:35], s[12:13] op_sel_hi:[1,0]
	v_pk_mul_f32 v[8:9], v[32:33], s[12:13] op_sel_hi:[1,0]
	v_pk_fma_f32 v[16:17], v[124:125], s[34:35], v[6:7] op_sel_hi:[1,0,1]
	v_pk_fma_f32 v[6:7], v[122:123], s[34:35], v[8:9] op_sel_hi:[1,0,1]
	v_pk_mul_f32 v[8:9], v[22:23], s[12:13] op_sel_hi:[1,0]
	v_cvt_pk_bf16_f32 v6, v6, v7
	v_pk_fma_f32 v[20:21], v[120:121], s[34:35], v[8:9] op_sel_hi:[1,0,1]
	v_pk_fma_f32 v[8:9], v[118:119], s[34:35], v[18:19] op_sel_hi:[1,0,1]
	v_cvt_pk_bf16_f32 v7, v16, v17
	v_cvt_pk_bf16_f32 v8, v8, v9
	v_cvt_pk_bf16_f32 v9, v20, v21
	global_store_dwordx4 v[14:15], v[6:9], off offset:256
	v_lshlrev_b64 v[14:15], 11, v[24:25]
	s_waitcnt vmcnt(5)
	v_pk_mul_f32 v[18:19], v[180:181], s[12:13] op_sel_hi:[1,0]
	s_waitcnt vmcnt(4)
	v_pk_mul_f32 v[6:7], v[186:187], s[12:13] op_sel_hi:[1,0]
	v_pk_mul_f32 v[8:9], v[184:185], s[12:13] op_sel_hi:[1,0]
	v_pk_fma_f32 v[16:17], v[116:117], s[34:35], v[6:7] op_sel_hi:[1,0,1]
	v_pk_fma_f32 v[6:7], v[114:115], s[34:35], v[8:9] op_sel_hi:[1,0,1]
	v_pk_mul_f32 v[8:9], v[182:183], s[12:13] op_sel_hi:[1,0]
	v_lshl_add_u64 v[14:15], s[44:45], 0, v[14:15]
	v_pk_fma_f32 v[20:21], v[112:113], s[34:35], v[8:9] op_sel_hi:[1,0,1]
	v_pk_fma_f32 v[8:9], v[110:111], s[34:35], v[18:19] op_sel_hi:[1,0,1]
	v_cvt_pk_bf16_f32 v6, v6, v7
	v_cvt_pk_bf16_f32 v7, v16, v17
	v_cvt_pk_bf16_f32 v8, v8, v9
	v_cvt_pk_bf16_f32 v9, v20, v21
	v_lshl_add_u64 v[14:15], v[14:15], 0, v[26:27]
	global_store_dwordx4 v[14:15], v[6:9], off
	s_waitcnt vmcnt(4)
	v_pk_mul_f32 v[18:19], v[190:191], s[12:13] op_sel_hi:[1,0]
	s_waitcnt vmcnt(3)
	v_pk_mul_f32 v[6:7], v[196:197], s[12:13] op_sel_hi:[1,0]
	v_pk_mul_f32 v[8:9], v[194:195], s[12:13] op_sel_hi:[1,0]
	v_pk_fma_f32 v[16:17], v[100:101], s[34:35], v[6:7] op_sel_hi:[1,0,1]
	v_pk_fma_f32 v[6:7], v[98:99], s[34:35], v[8:9] op_sel_hi:[1,0,1]
	v_pk_mul_f32 v[8:9], v[192:193], s[12:13] op_sel_hi:[1,0]
	v_cvt_pk_bf16_f32 v6, v6, v7
	v_pk_fma_f32 v[20:21], v[92:93], s[34:35], v[8:9] op_sel_hi:[1,0,1]
	v_pk_fma_f32 v[8:9], v[90:91], s[34:35], v[18:19] op_sel_hi:[1,0,1]
	v_cvt_pk_bf16_f32 v7, v16, v17
	v_cvt_pk_bf16_f32 v8, v8, v9
	v_cvt_pk_bf16_f32 v9, v20, v21
	global_store_dwordx4 v[14:15], v[6:9], off offset:256
	v_add_u32_e32 v14, 0x80, v10
	v_ashrrev_i32_e32 v15, 31, v14
	v_lshlrev_b64 v[6:7], 12, v[14:15]
	v_lshl_add_u64 v[24:25], v[12:13], 0, v[6:7]
	global_load_dwordx4 v[6:9], v[24:25], off offset:16
	global_load_dwordx4 v[16:19], v[24:25], off
	global_load_dwordx4 v[20:23], v[24:25], off offset:528
	global_load_dwordx4 v[32:35], v[24:25], off offset:512
	v_add_u32_e32 v24, 0x90, v10
	v_ashrrev_i32_e32 v25, 31, v24
	v_lshlrev_b64 v[36:37], 12, v[24:25]
	v_lshl_add_u64 v[36:37], v[12:13], 0, v[36:37]
	global_load_dwordx4 v[180:183], v[36:37], off offset:16
	global_load_dwordx4 v[184:187], v[36:37], off
	global_load_dwordx4 v[190:193], v[36:37], off offset:528
	global_load_dwordx4 v[194:197], v[36:37], off offset:512
	v_lshlrev_b64 v[14:15], 11, v[14:15]
	v_lshl_add_u64 v[14:15], s[44:45], 0, v[14:15]
	v_lshl_add_u64 v[14:15], v[14:15], 0, v[26:27]
	s_waitcnt vmcnt(7)
	v_pk_mul_f32 v[8:9], v[8:9], s[12:13] op_sel_hi:[1,0]
	s_waitcnt vmcnt(6)
	v_pk_mul_f32 v[18:19], v[18:19], s[12:13] op_sel_hi:[1,0]
	v_pk_mul_f32 v[16:17], v[16:17], s[12:13] op_sel_hi:[1,0]
	v_pk_mul_f32 v[6:7], v[6:7], s[12:13] op_sel_hi:[1,0]
	v_pk_fma_f32 v[18:19], v[108:109], s[34:35], v[18:19] op_sel_hi:[1,0,1]
	v_pk_fma_f32 v[16:17], v[106:107], s[34:35], v[16:17] op_sel_hi:[1,0,1]
	v_pk_fma_f32 v[36:37], v[104:105], s[34:35], v[8:9] op_sel_hi:[1,0,1]
	v_pk_fma_f32 v[8:9], v[102:103], s[34:35], v[6:7] op_sel_hi:[1,0,1]
	v_cvt_pk_bf16_f32 v6, v16, v17
	v_cvt_pk_bf16_f32 v7, v18, v19
	v_cvt_pk_bf16_f32 v8, v8, v9
	v_cvt_pk_bf16_f32 v9, v36, v37
	global_store_dwordx4 v[14:15], v[6:9], off
	s_waitcnt vmcnt(6)
	v_pk_mul_f32 v[18:19], v[20:21], s[12:13] op_sel_hi:[1,0]
	s_waitcnt vmcnt(5)
	v_pk_mul_f32 v[6:7], v[34:35], s[12:13] op_sel_hi:[1,0]
	v_pk_mul_f32 v[8:9], v[32:33], s[12:13] op_sel_hi:[1,0]
	v_pk_fma_f32 v[16:17], v[96:97], s[34:35], v[6:7] op_sel_hi:[1,0,1]
	v_pk_fma_f32 v[6:7], v[94:95], s[34:35], v[8:9] op_sel_hi:[1,0,1]
	v_pk_mul_f32 v[8:9], v[22:23], s[12:13] op_sel_hi:[1,0]
	v_cvt_pk_bf16_f32 v6, v6, v7
	v_pk_fma_f32 v[20:21], v[88:89], s[34:35], v[8:9] op_sel_hi:[1,0,1]
	v_pk_fma_f32 v[8:9], v[86:87], s[34:35], v[18:19] op_sel_hi:[1,0,1]
	v_cvt_pk_bf16_f32 v7, v16, v17
	v_cvt_pk_bf16_f32 v8, v8, v9
	v_cvt_pk_bf16_f32 v9, v20, v21
	global_store_dwordx4 v[14:15], v[6:9], off offset:256
	v_lshlrev_b64 v[14:15], 11, v[24:25]
	s_waitcnt vmcnt(5)
	v_pk_mul_f32 v[18:19], v[180:181], s[12:13] op_sel_hi:[1,0]
	s_waitcnt vmcnt(4)
; #define GAS __attribute__((address_space(1)))
; DI u32x4 pack8(const f32x4& v0, const f32x4& v1) { u32x4 w; w.x = cvt_pk_bf16(v0[0], v0[1]); w.y = cvt_pk_bf16(v0[2], v0[3]); w.z = cvt_pk_bf16(v1[0], v1[1]); w.w = cvt_pk_bf16(v1[2], v1[3]); return w; }
;     DI void operator()(const f32x4 (&acc)[2][2][4][2], const Unit& u, int wr, int wc, int fr, int fq) const {
;     ...
;                 for (int m2 = 0; m2 < 4; m2 += 2) { f32x4 a[2][2][2];
; #pragma unroll
;                     for (int mm = 0; mm < 2; ++mm)
; #pragma unroll
;                         for (int bj = 0; bj < 2; ++bj) { const size_t off = (size_t)(row0 + ai * 128 + (m2 + mm) * 16) * 1024 + col0 + bj * 128; a[mm][bj][0] = *(const GAS f32x4*)(x32 + off); a[mm][bj][1] = *(const GAS f32x4*)(x32 + off + 4); }
;                     asm volatile("" ::: "memory");
; #pragma unroll
;                     for (int mm = 0; mm < 2; ++mm)
; #pragma unroll
;                         for (int bj = 0; bj < 2; ++bj) { const size_t off = (size_t)(row0 + ai * 128 + (m2 + mm) * 16) * 1024 + col0 + bj * 128;
;                             *(GAS u32x4*)(xr + off) = pack8(a[mm][bj][0] * DN_ALPHA + acc[ai][bj][m2 + mm][0] * W8_INV, a[mm][bj][1] * DN_ALPHA + acc[ai][bj][m2 + mm][1] * W8_INV); }
;                     asm volatile("" ::: "memory"); }
	v_pk_mul_f32 v[6:7], v[186:187], s[12:13] op_sel_hi:[1,0]
	v_pk_mul_f32 v[8:9], v[184:185], s[12:13] op_sel_hi:[1,0]
	v_pk_fma_f32 v[16:17], v[84:85], s[34:35], v[6:7] op_sel_hi:[1,0,1]
	v_pk_fma_f32 v[6:7], v[82:83], s[34:35], v[8:9] op_sel_hi:[1,0,1]
	v_pk_mul_f32 v[8:9], v[182:183], s[12:13] op_sel_hi:[1,0]
	v_lshl_add_u64 v[14:15], s[44:45], 0, v[14:15]
	v_pk_fma_f32 v[20:21], v[80:81], s[34:35], v[8:9] op_sel_hi:[1,0,1]
	v_pk_fma_f32 v[8:9], v[78:79], s[34:35], v[18:19] op_sel_hi:[1,0,1]
	v_cvt_pk_bf16_f32 v6, v6, v7
	v_cvt_pk_bf16_f32 v7, v16, v17
	v_cvt_pk_bf16_f32 v8, v8, v9
	v_cvt_pk_bf16_f32 v9, v20, v21
	v_lshl_add_u64 v[14:15], v[14:15], 0, v[26:27]
	global_store_dwordx4 v[14:15], v[6:9], off
	s_waitcnt vmcnt(4)
	v_pk_mul_f32 v[18:19], v[190:191], s[12:13] op_sel_hi:[1,0]
	v_add_u32_e32 v24, 0xb0, v10
	s_waitcnt vmcnt(3)
	v_pk_mul_f32 v[6:7], v[196:197], s[12:13] op_sel_hi:[1,0]
	v_pk_mul_f32 v[8:9], v[194:195], s[12:13] op_sel_hi:[1,0]
	v_pk_fma_f32 v[16:17], v[76:77], s[34:35], v[6:7] op_sel_hi:[1,0,1]
	v_pk_fma_f32 v[6:7], v[74:75], s[34:35], v[8:9] op_sel_hi:[1,0,1]
	v_pk_mul_f32 v[8:9], v[192:193], s[12:13] op_sel_hi:[1,0]
	v_cvt_pk_bf16_f32 v6, v6, v7
	v_pk_fma_f32 v[20:21], v[72:73], s[34:35], v[8:9] op_sel_hi:[1,0,1]
	v_pk_fma_f32 v[8:9], v[70:71], s[34:35], v[18:19] op_sel_hi:[1,0,1]
	v_add_u32_e32 v18, 0xa0, v10
	v_cvt_pk_bf16_f32 v7, v16, v17
	v_cvt_pk_bf16_f32 v8, v8, v9
	v_cvt_pk_bf16_f32 v9, v20, v21
	v_ashrrev_i32_e32 v19, 31, v18
	global_store_dwordx4 v[14:15], v[6:9], off offset:256
	v_ashrrev_i32_e32 v25, 31, v24
	s_nop 0
	v_lshlrev_b64 v[6:7], 12, v[18:19]
	v_lshl_add_u64 v[6:7], v[12:13], 0, v[6:7]
	global_load_dwordx4 v[14:17], v[6:7], off offset:16
	global_load_dwordx4 v[20:23], v[6:7], off
	global_load_dwordx4 v[32:35], v[6:7], off offset:528
	global_load_dwordx4 v[180:183], v[6:7], off offset:512
	v_lshlrev_b64 v[6:7], 12, v[24:25]
	v_lshl_add_u64 v[10:11], v[12:13], 0, v[6:7]
	global_load_dwordx4 v[184:187], v[10:11], off offset:16
	global_load_dwordx4 v[190:193], v[10:11], off
	global_load_dwordx4 v[6:9], v[10:11], off offset:528
	s_nop 0
	global_load_dwordx4 v[10:13], v[10:11], off offset:512
	v_lshlrev_b64 v[18:19], 11, v[18:19]
	v_lshl_add_u64 v[18:19], s[44:45], 0, v[18:19]
	v_lshl_add_u64 v[18:19], v[18:19], 0, v[26:27]
	s_waitcnt vmcnt(7)
	v_pk_mul_f32 v[16:17], v[16:17], s[12:13] op_sel_hi:[1,0]
	s_waitcnt vmcnt(6)
	v_pk_mul_f32 v[22:23], v[22:23], s[12:13] op_sel_hi:[1,0]
	v_pk_mul_f32 v[20:21], v[20:21], s[12:13] op_sel_hi:[1,0]
	v_pk_mul_f32 v[14:15], v[14:15], s[12:13] op_sel_hi:[1,0]
	v_pk_fma_f32 v[22:23], v[68:69], s[34:35], v[22:23] op_sel_hi:[1,0,1]
	v_pk_fma_f32 v[20:21], v[66:67], s[34:35], v[20:21] op_sel_hi:[1,0,1]
	v_pk_fma_f32 v[36:37], v[64:65], s[34:35], v[16:17] op_sel_hi:[1,0,1]
	v_pk_fma_f32 v[16:17], v[62:63], s[34:35], v[14:15] op_sel_hi:[1,0,1]
	v_cvt_pk_bf16_f32 v14, v20, v21
	v_cvt_pk_bf16_f32 v15, v22, v23
	v_cvt_pk_bf16_f32 v16, v16, v17
	v_cvt_pk_bf16_f32 v17, v36, v37
	global_store_dwordx4 v[18:19], v[14:17], off
	s_waitcnt vmcnt(6)
	v_pk_mul_f32 v[22:23], v[32:33], s[12:13] op_sel_hi:[1,0]
	s_waitcnt vmcnt(1)
	v_pk_mul_f32 v[12:13], v[12:13], s[12:13] op_sel_hi:[1,0]
	v_pk_mul_f32 v[14:15], v[182:183], s[12:13] op_sel_hi:[1,0]
	v_pk_mul_f32 v[16:17], v[180:181], s[12:13] op_sel_hi:[1,0]
	v_pk_fma_f32 v[20:21], v[60:61], s[34:35], v[14:15] op_sel_hi:[1,0,1]
	v_pk_fma_f32 v[14:15], v[58:59], s[34:35], v[16:17] op_sel_hi:[1,0,1]
	v_pk_mul_f32 v[16:17], v[34:35], s[12:13] op_sel_hi:[1,0]
	v_cvt_pk_bf16_f32 v14, v14, v15
	v_pk_fma_f32 v[32:33], v[56:57], s[34:35], v[16:17] op_sel_hi:[1,0,1]
	v_pk_fma_f32 v[16:17], v[54:55], s[34:35], v[22:23] op_sel_hi:[1,0,1]
	v_cvt_pk_bf16_f32 v15, v20, v21
	v_cvt_pk_bf16_f32 v16, v16, v17
	v_cvt_pk_bf16_f32 v17, v32, v33
	global_store_dwordx4 v[18:19], v[14:17], off offset:256
	v_lshlrev_b64 v[18:19], 11, v[24:25]
	v_pk_mul_f32 v[22:23], v[184:185], s[12:13] op_sel_hi:[1,0]
	v_pk_mul_f32 v[14:15], v[192:193], s[12:13] op_sel_hi:[1,0]
	v_pk_mul_f32 v[16:17], v[190:191], s[12:13] op_sel_hi:[1,0]
	v_pk_fma_f32 v[20:21], v[52:53], s[34:35], v[14:15] op_sel_hi:[1,0,1]
	v_pk_fma_f32 v[14:15], v[50:51], s[34:35], v[16:17] op_sel_hi:[1,0,1]
	v_pk_mul_f32 v[16:17], v[186:187], s[12:13] op_sel_hi:[1,0]
	v_lshl_add_u64 v[18:19], s[44:45], 0, v[18:19]
	v_pk_fma_f32 v[24:25], v[48:49], s[34:35], v[16:17] op_sel_hi:[1,0,1]
	v_pk_fma_f32 v[16:17], v[46:47], s[34:35], v[22:23] op_sel_hi:[1,0,1]
	v_cvt_pk_bf16_f32 v14, v14, v15
	v_cvt_pk_bf16_f32 v15, v20, v21
	v_cvt_pk_bf16_f32 v16, v16, v17
	v_cvt_pk_bf16_f32 v17, v24, v25
	v_lshl_add_u64 v[18:19], v[18:19], 0, v[26:27]
	v_pk_mul_f32 v[10:11], v[10:11], s[12:13] op_sel_hi:[1,0]
	v_pk_mul_f32 v[8:9], v[8:9], s[12:13] op_sel_hi:[1,0]
	v_pk_mul_f32 v[6:7], v[6:7], s[12:13] op_sel_hi:[1,0]
	global_store_dwordx4 v[18:19], v[14:17], off
	v_pk_fma_f32 v[12:13], v[44:45], s[34:35], v[12:13] op_sel_hi:[1,0,1]
	v_pk_fma_f32 v[10:11], v[42:43], s[34:35], v[10:11] op_sel_hi:[1,0,1]
	v_pk_fma_f32 v[14:15], v[40:41], s[34:35], v[8:9] op_sel_hi:[1,0,1]
	v_pk_fma_f32 v[8:9], v[38:39], s[34:35], v[6:7] op_sel_hi:[1,0,1]
	v_cvt_pk_bf16_f32 v6, v10, v11
	v_cvt_pk_bf16_f32 v7, v12, v13
	v_cvt_pk_bf16_f32 v8, v8, v9
	v_cvt_pk_bf16_f32 v9, v14, v15
	global_store_dwordx4 v[18:19], v[6:9], off offset:256
	s_cbranch_execnz .LBB0_1049

; DI unsigned pk4_fp8(float a, float b, float c_, float d) { int w = 0; w = __builtin_amdgcn_cvt_pk_fp8_f32(clamp8(a), clamp8(b), w, false); w = __builtin_amdgcn_cvt_pk_fp8_f32(clamp8(c_), clamp8(d), w, true); return (unsigned)w; }
; DI float sigmoid64_(float x64) { return __builtin_amdgcn_rcpf(1.0f + __builtin_amdgcn_exp2f(x64 * (-LOG2E * W8_INV))); }
;     DI void operator()(const f32x4 (&acc)[2][2][4][2], const Unit& u, int wr, int wc, int fr, int fq) const {
;     ...
;         const int row0 = u.pm * 256 + wr * 64 + fr, col0 = u.pn * 128 + wc * 32 + 8 * fq;
; #pragma unroll
;         for (int ai = 0; ai < 2; ++ai)
; #pragma unroll
;             for (int m2 = 0; m2 < 4; m2 += 2) { u32x2 o[2];
; #pragma unroll
;                 for (int mm = 0; mm < 2; ++mm) { const int m = m2 + mm; f32x4 v0, v1;
; #pragma unroll
;                     for (int j = 0; j < 4; ++j) { const float g0 = acc[ai][0][m][0][j], g1 = acc[ai][0][m][1][j]; v0[j] = g0 * sigmoid64_(g0) * (acc[ai][1][m][0][j] * (W8_INV * W8_INV)); v1[j] = g1 * sigmoid64_(g1) * (acc[ai][1][m][1][j] * (W8_INV * W8_INV)); }
;                     o[mm].x = pk4_fp8(v0[0], v0[1], v0[2], v0[3]); o[mm].y = pk4_fp8(v1[0], v1[1], v1[2], v1[3]); }
;                 st_pair16(hm + (size_t)(row0 + ai * 128 + m2 * 16) * 1024 + col0, 16 * 1024, o[0], o[1], fq); }
.LBB0_1367:
	s_nop 15
	s_lshl_b32 s6, s90, 8
	s_add_i32 s6, s6, s68
	v_add_u32_e32 v12, s6, v237
	s_lshl_b32 s6, s54, 7
	s_or_b32 s6, s6, s80
	v_lshl_add_u32 v14, v238, 3, s6
	v_bfe_i32 v6, v238, 0, 1
	v_and_b32_e32 v10, 0x3ff8, v6
	v_mov_b32_e32 v11, v4
	v_ashrrev_i32_e32 v15, 31, v14
	v_ashrrev_i32_e32 v13, 31, v12
	v_lshlrev_b64 v[12:13], 10, v[12:13]
	v_lshl_add_u64 v[12:13], s[46:47], 0, v[12:13]
	v_lshl_add_u64 v[12:13], v[12:13], 0, v[14:15]
	v_lshl_add_u64 v[10:11], v[12:13], 0, v[10:11]
	s_mov_b32 s6, 0x8000
	s_mov_b64 s[54:55], -1
	v_mov_b32_e32 v20, 1.0
	v_mov_b32_e32 v21, 1.0
	v_mul_f32_e32 v16, 0xbcb8aa3b, v190
	v_mul_f32_e32 v17, 0xbcb8aa3b, v191
	v_mul_f32_e32 v18, 0xbcb8aa3b, v192
	v_mul_f32_e32 v19, 0xbcb8aa3b, v193
	v_exp_f32_e32 v16, v16
	v_exp_f32_e32 v17, v17
	v_exp_f32_e32 v18, v18
	v_exp_f32_e32 v19, v19
	v_pk_add_f32 v[16:17], v[16:17], v[20:21]
	v_pk_add_f32 v[18:19], v[18:19], v[20:21]
	v_rcp_f32_e32 v16, v16
	v_rcp_f32_e32 v17, v17
	v_rcp_f32_e32 v18, v18
	v_rcp_f32_e32 v19, v19
	v_pk_mul_f32 v[194:195], v[194:195], v[206:207] op_sel:[0,1] op_sel_hi:[1,1]
	v_pk_mul_f32 v[196:197], v[196:197], v[206:207] op_sel:[0,1] op_sel_hi:[1,1]
	v_pk_mul_f32 v[190:191], v[190:191], v[16:17]
	v_pk_mul_f32 v[192:193], v[192:193], v[18:19]
	v_pk_mul_f32 v[190:191], v[190:191], v[194:195]
	v_pk_mul_f32 v[192:193], v[192:193], v[196:197]
	v_med3_f32 v190, v190, s35, v225
	v_med3_f32 v191, v191, s35, v225
	v_med3_f32 v192, v192, s35, v225
	v_med3_f32 v193, v193, s35, v225
	v_mul_f32_e32 v16, 0xbcb8aa3b, v182
	v_mul_f32_e32 v17, 0xbcb8aa3b, v183
	v_mul_f32_e32 v18, 0xbcb8aa3b, v184
	v_mul_f32_e32 v19, 0xbcb8aa3b, v185
	v_exp_f32_e32 v16, v16
	v_exp_f32_e32 v17, v17
	v_exp_f32_e32 v18, v18
	v_exp_f32_e32 v19, v19
	v_pk_add_f32 v[16:17], v[16:17], v[20:21]
	v_pk_add_f32 v[18:19], v[18:19], v[20:21]
	v_rcp_f32_e32 v16, v16
	v_rcp_f32_e32 v17, v17
	v_rcp_f32_e32 v18, v18
	v_rcp_f32_e32 v19, v19
	v_pk_mul_f32 v[186:187], v[186:187], v[206:207] op_sel:[0,1] op_sel_hi:[1,1]
	v_pk_mul_f32 v[188:189], v[188:189], v[206:207] op_sel:[0,1] op_sel_hi:[1,1]
	v_pk_mul_f32 v[182:183], v[182:183], v[16:17]
	v_pk_mul_f32 v[184:185], v[184:185], v[18:19]
	v_pk_mul_f32 v[182:183], v[182:183], v[186:187]
	v_pk_mul_f32 v[184:185], v[184:185], v[188:189]
	v_med3_f32 v182, v182, s35, v225
	v_med3_f32 v183, v183, s35, v225
	v_med3_f32 v184, v184, s35, v225
	v_med3_f32 v185, v185, s35, v225
	v_mul_f32_e32 v16, 0xbcb8aa3b, v174
	v_mul_f32_e32 v17, 0xbcb8aa3b, v175
	v_mul_f32_e32 v18, 0xbcb8aa3b, v176
	v_mul_f32_e32 v19, 0xbcb8aa3b, v177
	v_exp_f32_e32 v16, v16
	v_exp_f32_e32 v17, v17
	v_exp_f32_e32 v18, v18
	v_exp_f32_e32 v19, v19
	v_pk_add_f32 v[16:17], v[16:17], v[20:21]
	v_pk_add_f32 v[18:19], v[18:19], v[20:21]
	v_rcp_f32_e32 v16, v16
	v_rcp_f32_e32 v17, v17
	v_rcp_f32_e32 v18, v18
	v_rcp_f32_e32 v19, v19
	v_pk_mul_f32 v[178:179], v[178:179], v[206:207] op_sel:[0,1] op_sel_hi:[1,1]
	v_pk_mul_f32 v[180:181], v[180:181], v[206:207] op_sel:[0,1] op_sel_hi:[1,1]
	v_pk_mul_f32 v[174:175], v[174:175], v[16:17]
	v_pk_mul_f32 v[176:177], v[176:177], v[18:19]
	v_pk_mul_f32 v[174:175], v[174:175], v[178:179]
	v_pk_mul_f32 v[176:177], v[176:177], v[180:181]
	v_med3_f32 v174, v174, s35, v225
	v_med3_f32 v175, v175, s35, v225
	v_med3_f32 v176, v176, s35, v225
	v_med3_f32 v177, v177, s35, v225
	v_mul_f32_e32 v16, 0xbcb8aa3b, v166
	v_mul_f32_e32 v17, 0xbcb8aa3b, v167
	v_mul_f32_e32 v18, 0xbcb8aa3b, v168
	v_mul_f32_e32 v19, 0xbcb8aa3b, v169
	v_exp_f32_e32 v16, v16
	v_exp_f32_e32 v17, v17
	v_exp_f32_e32 v18, v18
	v_exp_f32_e32 v19, v19
	v_pk_add_f32 v[16:17], v[16:17], v[20:21]
	v_pk_add_f32 v[18:19], v[18:19], v[20:21]
	v_rcp_f32_e32 v16, v16
	v_rcp_f32_e32 v17, v17
	v_rcp_f32_e32 v18, v18
	v_rcp_f32_e32 v19, v19
	v_pk_mul_f32 v[170:171], v[170:171], v[206:207] op_sel:[0,1] op_sel_hi:[1,1]
	v_pk_mul_f32 v[172:173], v[172:173], v[206:207] op_sel:[0,1] op_sel_hi:[1,1]
	v_pk_mul_f32 v[166:167], v[166:167], v[16:17]
	v_pk_mul_f32 v[168:169], v[168:169], v[18:19]
	v_pk_mul_f32 v[166:167], v[166:167], v[170:171]
	v_pk_mul_f32 v[168:169], v[168:169], v[172:173]
	v_med3_f32 v166, v166, s35, v225
	v_med3_f32 v167, v167, s35, v225
	v_med3_f32 v168, v168, s35, v225
	v_med3_f32 v169, v169, s35, v225
	v_cvt_pk_fp8_f32 v190, v190, v191
	v_cvt_pk_fp8_f32 v191, v182, v183
	v_cvt_pk_fp8_f32 v190, v192, v193 op_sel:[0,0,1]
	v_cvt_pk_fp8_f32 v191, v184, v185 op_sel:[0,0,1]
	v_cvt_pk_fp8_f32 v192, v174, v175
	v_cvt_pk_fp8_f32 v193, v166, v167
	v_cvt_pk_fp8_f32 v192, v176, v177 op_sel:[0,0,1]
	v_cvt_pk_fp8_f32 v193, v168, v169 op_sel:[0,0,1]
	s_nop 1
	v_permlane16_swap_b32_e32 v190, v192
	v_permlane16_swap_b32_e32 v191, v193
	global_store_dwordx4 v[10:11], v[190:193], off
	v_mul_f32_e32 v16, 0xbcb8aa3b, v158
	v_mul_f32_e32 v17, 0xbcb8aa3b, v159
	v_mul_f32_e32 v18, 0xbcb8aa3b, v160
	v_mul_f32_e32 v19, 0xbcb8aa3b, v161
	v_exp_f32_e32 v16, v16
	v_exp_f32_e32 v17, v17
	v_exp_f32_e32 v18, v18
	v_exp_f32_e32 v19, v19
	v_pk_add_f32 v[16:17], v[16:17], v[20:21]
	v_pk_add_f32 v[18:19], v[18:19], v[20:21]
	v_rcp_f32_e32 v16, v16
	v_rcp_f32_e32 v17, v17
	v_rcp_f32_e32 v18, v18
	v_rcp_f32_e32 v19, v19
	v_pk_mul_f32 v[162:163], v[162:163], v[206:207] op_sel:[0,1] op_sel_hi:[1,1]
	v_pk_mul_f32 v[164:165], v[164:165], v[206:207] op_sel:[0,1] op_sel_hi:[1,1]
	v_pk_mul_f32 v[158:159], v[158:159], v[16:17]
	v_pk_mul_f32 v[160:161], v[160:161], v[18:19]
	v_pk_mul_f32 v[158:159], v[158:159], v[162:163]
	v_pk_mul_f32 v[160:161], v[160:161], v[164:165]
	v_med3_f32 v158, v158, s35, v225
	v_med3_f32 v159, v159, s35, v225
	v_med3_f32 v160, v160, s35, v225
	v_med3_f32 v161, v161, s35, v225
	v_mul_f32_e32 v16, 0xbcb8aa3b, v150
; DI unsigned pk4_fp8(float a, float b, float c_, float d) { int w = 0; w = __builtin_amdgcn_cvt_pk_fp8_f32(clamp8(a), clamp8(b), w, false); w = __builtin_amdgcn_cvt_pk_fp8_f32(clamp8(c_), clamp8(d), w, true); return (unsigned)w; }
; DI float sigmoid64_(float x64) { return __builtin_amdgcn_rcpf(1.0f + __builtin_amdgcn_exp2f(x64 * (-LOG2E * W8_INV))); }
;     DI void operator()(const f32x4 (&acc)[2][2][4][2], const Unit& u, int wr, int wc, int fr, int fq) const {
;     ...
;         const int row0 = u.pm * 256 + wr * 64 + fr, col0 = u.pn * 128 + wc * 32 + 8 * fq;
; #pragma unroll
;         for (int ai = 0; ai < 2; ++ai)
; #pragma unroll
;             for (int m2 = 0; m2 < 4; m2 += 2) { u32x2 o[2];
; #pragma unroll
;                 for (int mm = 0; mm < 2; ++mm) { const int m = m2 + mm; f32x4 v0, v1;
; #pragma unroll
;                     for (int j = 0; j < 4; ++j) { const float g0 = acc[ai][0][m][0][j], g1 = acc[ai][0][m][1][j]; v0[j] = g0 * sigmoid64_(g0) * (acc[ai][1][m][0][j] * (W8_INV * W8_INV)); v1[j] = g1 * sigmoid64_(g1) * (acc[ai][1][m][1][j] * (W8_INV * W8_INV)); }
;                     o[mm].x = pk4_fp8(v0[0], v0[1], v0[2], v0[3]); o[mm].y = pk4_fp8(v1[0], v1[1], v1[2], v1[3]); }
;                 st_pair16(hm + (size_t)(row0 + ai * 128 + m2 * 16) * 1024 + col0, 16 * 1024, o[0], o[1], fq); }
	v_mul_f32_e32 v17, 0xbcb8aa3b, v151
	v_mul_f32_e32 v18, 0xbcb8aa3b, v152
	v_mul_f32_e32 v19, 0xbcb8aa3b, v153
	v_exp_f32_e32 v16, v16
	v_exp_f32_e32 v17, v17
	v_exp_f32_e32 v18, v18
	v_exp_f32_e32 v19, v19
	v_pk_add_f32 v[16:17], v[16:17], v[20:21]
	v_pk_add_f32 v[18:19], v[18:19], v[20:21]
	v_rcp_f32_e32 v16, v16
	v_rcp_f32_e32 v17, v17
	v_rcp_f32_e32 v18, v18
	v_rcp_f32_e32 v19, v19
	v_pk_mul_f32 v[154:155], v[154:155], v[206:207] op_sel:[0,1] op_sel_hi:[1,1]
	v_pk_mul_f32 v[156:157], v[156:157], v[206:207] op_sel:[0,1] op_sel_hi:[1,1]
	v_pk_mul_f32 v[150:151], v[150:151], v[16:17]
	v_pk_mul_f32 v[152:153], v[152:153], v[18:19]
	v_pk_mul_f32 v[150:151], v[150:151], v[154:155]
	v_pk_mul_f32 v[152:153], v[152:153], v[156:157]
	v_med3_f32 v150, v150, s35, v225
	v_med3_f32 v151, v151, s35, v225
	v_med3_f32 v152, v152, s35, v225
	v_med3_f32 v153, v153, s35, v225
	v_mul_f32_e32 v16, 0xbcb8aa3b, v142
	v_mul_f32_e32 v17, 0xbcb8aa3b, v143
	v_mul_f32_e32 v18, 0xbcb8aa3b, v144
	v_mul_f32_e32 v19, 0xbcb8aa3b, v145
	v_exp_f32_e32 v16, v16
	v_exp_f32_e32 v17, v17
	v_exp_f32_e32 v18, v18
	v_exp_f32_e32 v19, v19
	v_pk_add_f32 v[16:17], v[16:17], v[20:21]
	v_pk_add_f32 v[18:19], v[18:19], v[20:21]
	v_rcp_f32_e32 v16, v16
	v_rcp_f32_e32 v17, v17
	v_rcp_f32_e32 v18, v18
	v_rcp_f32_e32 v19, v19
	v_pk_mul_f32 v[146:147], v[146:147], v[206:207] op_sel:[0,1] op_sel_hi:[1,1]
	v_pk_mul_f32 v[148:149], v[148:149], v[206:207] op_sel:[0,1] op_sel_hi:[1,1]
	v_pk_mul_f32 v[142:143], v[142:143], v[16:17]
	v_pk_mul_f32 v[144:145], v[144:145], v[18:19]
	v_pk_mul_f32 v[142:143], v[142:143], v[146:147]
	v_pk_mul_f32 v[144:145], v[144:145], v[148:149]
	v_med3_f32 v142, v142, s35, v225
	v_med3_f32 v143, v143, s35, v225
	v_med3_f32 v144, v144, s35, v225
	v_med3_f32 v145, v145, s35, v225
	v_mul_f32_e32 v16, 0xbcb8aa3b, v134
	v_mul_f32_e32 v17, 0xbcb8aa3b, v135
	v_mul_f32_e32 v18, 0xbcb8aa3b, v136
	v_mul_f32_e32 v19, 0xbcb8aa3b, v137
	v_exp_f32_e32 v16, v16
	v_exp_f32_e32 v17, v17
	v_exp_f32_e32 v18, v18
	v_exp_f32_e32 v19, v19
	v_pk_add_f32 v[16:17], v[16:17], v[20:21]
	v_pk_add_f32 v[18:19], v[18:19], v[20:21]
	v_rcp_f32_e32 v16, v16
	v_rcp_f32_e32 v17, v17
	v_rcp_f32_e32 v18, v18
	v_rcp_f32_e32 v19, v19
	v_pk_mul_f32 v[138:139], v[138:139], v[206:207] op_sel:[0,1] op_sel_hi:[1,1]
	v_pk_mul_f32 v[140:141], v[140:141], v[206:207] op_sel:[0,1] op_sel_hi:[1,1]
	v_pk_mul_f32 v[134:135], v[134:135], v[16:17]
	v_pk_mul_f32 v[136:137], v[136:137], v[18:19]
	v_pk_mul_f32 v[134:135], v[134:135], v[138:139]
	v_pk_mul_f32 v[136:137], v[136:137], v[140:141]
	v_med3_f32 v134, v134, s35, v225
	v_med3_f32 v135, v135, s35, v225
	v_med3_f32 v136, v136, s35, v225
	v_med3_f32 v137, v137, s35, v225
	v_cvt_pk_fp8_f32 v158, v158, v159
	v_cvt_pk_fp8_f32 v159, v150, v151
	v_cvt_pk_fp8_f32 v158, v160, v161 op_sel:[0,0,1]
	v_cvt_pk_fp8_f32 v159, v152, v153 op_sel:[0,0,1]
	v_cvt_pk_fp8_f32 v160, v142, v143
	v_cvt_pk_fp8_f32 v161, v134, v135
	v_cvt_pk_fp8_f32 v160, v144, v145 op_sel:[0,0,1]
	v_cvt_pk_fp8_f32 v161, v136, v137 op_sel:[0,0,1]
	v_add_co_u32_e32 v12, vcc, 0x8000, v10
	s_nop 0
	v_permlane16_swap_b32_e32 v158, v160
	v_addc_co_u32_e32 v13, vcc, 0, v11, vcc
	v_permlane16_swap_b32_e32 v159, v161
	global_store_dwordx4 v[12:13], v[158:161], off
	v_mul_f32_e32 v16, 0xbcb8aa3b, v126
	v_mul_f32_e32 v17, 0xbcb8aa3b, v127
	v_mul_f32_e32 v18, 0xbcb8aa3b, v128
	v_mul_f32_e32 v19, 0xbcb8aa3b, v129
	v_exp_f32_e32 v16, v16
	v_exp_f32_e32 v17, v17
	v_exp_f32_e32 v18, v18
	v_exp_f32_e32 v19, v19
	v_pk_add_f32 v[16:17], v[16:17], v[20:21]
	v_pk_add_f32 v[18:19], v[18:19], v[20:21]
	v_rcp_f32_e32 v16, v16
	v_rcp_f32_e32 v17, v17
	v_rcp_f32_e32 v18, v18
	v_rcp_f32_e32 v19, v19
	v_pk_mul_f32 v[130:131], v[130:131], v[206:207] op_sel:[0,1] op_sel_hi:[1,1]
	v_pk_mul_f32 v[132:133], v[132:133], v[206:207] op_sel:[0,1] op_sel_hi:[1,1]
	v_pk_mul_f32 v[126:127], v[126:127], v[16:17]
	v_pk_mul_f32 v[128:129], v[128:129], v[18:19]
	v_pk_mul_f32 v[126:127], v[126:127], v[130:131]
	v_pk_mul_f32 v[128:129], v[128:129], v[132:133]
	v_med3_f32 v126, v126, s35, v225
	v_med3_f32 v127, v127, s35, v225
	v_med3_f32 v128, v128, s35, v225
	v_med3_f32 v129, v129, s35, v225
	v_mul_f32_e32 v16, 0xbcb8aa3b, v118
	v_mul_f32_e32 v17, 0xbcb8aa3b, v119
	v_mul_f32_e32 v18, 0xbcb8aa3b, v120
	v_mul_f32_e32 v19, 0xbcb8aa3b, v121
	v_exp_f32_e32 v16, v16
	v_exp_f32_e32 v17, v17
	v_exp_f32_e32 v18, v18
	v_exp_f32_e32 v19, v19
	v_pk_add_f32 v[16:17], v[16:17], v[20:21]
	v_pk_add_f32 v[18:19], v[18:19], v[20:21]
	v_rcp_f32_e32 v16, v16
	v_rcp_f32_e32 v17, v17
	v_rcp_f32_e32 v18, v18
	v_rcp_f32_e32 v19, v19
	v_pk_mul_f32 v[122:123], v[122:123], v[206:207] op_sel:[0,1] op_sel_hi:[1,1]
	v_pk_mul_f32 v[124:125], v[124:125], v[206:207] op_sel:[0,1] op_sel_hi:[1,1]
	v_pk_mul_f32 v[118:119], v[118:119], v[16:17]
	v_pk_mul_f32 v[120:121], v[120:121], v[18:19]
	v_pk_mul_f32 v[118:119], v[118:119], v[122:123]
	v_pk_mul_f32 v[120:121], v[120:121], v[124:125]
	v_med3_f32 v118, v118, s35, v225
	v_med3_f32 v119, v119, s35, v225
	v_med3_f32 v120, v120, s35, v225
	v_med3_f32 v121, v121, s35, v225
	v_mul_f32_e32 v16, 0xbcb8aa3b, v110
	v_mul_f32_e32 v17, 0xbcb8aa3b, v111
	v_mul_f32_e32 v18, 0xbcb8aa3b, v112
	v_mul_f32_e32 v19, 0xbcb8aa3b, v113
	v_exp_f32_e32 v16, v16
	v_exp_f32_e32 v17, v17
	v_exp_f32_e32 v18, v18
	v_exp_f32_e32 v19, v19
	v_pk_add_f32 v[16:17], v[16:17], v[20:21]
	v_pk_add_f32 v[18:19], v[18:19], v[20:21]
	v_rcp_f32_e32 v16, v16
	v_rcp_f32_e32 v17, v17
	v_rcp_f32_e32 v18, v18
	v_rcp_f32_e32 v19, v19
	v_pk_mul_f32 v[114:115], v[114:115], v[206:207] op_sel:[0,1] op_sel_hi:[1,1]
	v_pk_mul_f32 v[116:117], v[116:117], v[206:207] op_sel:[0,1] op_sel_hi:[1,1]
; DI unsigned pk4_fp8(float a, float b, float c_, float d) { int w = 0; w = __builtin_amdgcn_cvt_pk_fp8_f32(clamp8(a), clamp8(b), w, false); w = __builtin_amdgcn_cvt_pk_fp8_f32(clamp8(c_), clamp8(d), w, true); return (unsigned)w; }
; DI float sigmoid64_(float x64) { return __builtin_amdgcn_rcpf(1.0f + __builtin_amdgcn_exp2f(x64 * (-LOG2E * W8_INV))); }
; #define PG8_BAR __builtin_amdgcn_s_barrier()
; template <class Epi, class Sched, bool F8 = false>
; DI void gemm_phase(LAS unsigned char* lds, const int K, const Sched& S, const Epi& E) {
;     ...
;         if (!has_next) break;
;         if constexpr (!F8)
; #pragma unroll
;         for (int a = 0; a < 2; ++a)
; #pragma unroll
;             for (int b = 0; b < 2; ++b)
; #pragma unroll
;                 for (int m = 0; m < 4; ++m)
; #pragma unroll
;                     for (int n = 0; n < 2; ++n) acc[a][b][m][n] = (f32x4){0.f, 0.f, 0.f, 0.f};
;         cur = nxt; cA = nA; cB = nB; ++ui;
;         if (wr == 1) PG8_BAR;
;     DI void operator()(const f32x4 (&acc)[2][2][4][2], const Unit& u, int wr, int wc, int fr, int fq) const {
;     ...
;         const int row0 = u.pm * 256 + wr * 64 + fr, col0 = u.pn * 128 + wc * 32 + 8 * fq;
; #pragma unroll
;         for (int ai = 0; ai < 2; ++ai)
; #pragma unroll
;             for (int m2 = 0; m2 < 4; m2 += 2) { u32x2 o[2];
; #pragma unroll
;                 for (int mm = 0; mm < 2; ++mm) { const int m = m2 + mm; f32x4 v0, v1;
; #pragma unroll
;                     for (int j = 0; j < 4; ++j) { const float g0 = acc[ai][0][m][0][j], g1 = acc[ai][0][m][1][j]; v0[j] = g0 * sigmoid64_(g0) * (acc[ai][1][m][0][j] * (W8_INV * W8_INV)); v1[j] = g1 * sigmoid64_(g1) * (acc[ai][1][m][1][j] * (W8_INV * W8_INV)); }
;                     o[mm].x = pk4_fp8(v0[0], v0[1], v0[2], v0[3]); o[mm].y = pk4_fp8(v1[0], v1[1], v1[2], v1[3]); }
;                 st_pair16(hm + (size_t)(row0 + ai * 128 + m2 * 16) * 1024 + col0, 16 * 1024, o[0], o[1], fq); }
	v_pk_mul_f32 v[110:111], v[110:111], v[16:17]
	v_pk_mul_f32 v[112:113], v[112:113], v[18:19]
	v_pk_mul_f32 v[110:111], v[110:111], v[114:115]
	v_pk_mul_f32 v[112:113], v[112:113], v[116:117]
	v_med3_f32 v110, v110, s35, v225
	v_med3_f32 v111, v111, s35, v225
	v_med3_f32 v112, v112, s35, v225
	v_med3_f32 v113, v113, s35, v225
	v_mul_f32_e32 v16, 0xbcb8aa3b, v102
	v_mul_f32_e32 v17, 0xbcb8aa3b, v103
	v_mul_f32_e32 v18, 0xbcb8aa3b, v104
	v_mul_f32_e32 v19, 0xbcb8aa3b, v105
	v_exp_f32_e32 v16, v16
	v_exp_f32_e32 v17, v17
	v_exp_f32_e32 v18, v18
	v_exp_f32_e32 v19, v19
	v_pk_add_f32 v[16:17], v[16:17], v[20:21]
	v_pk_add_f32 v[18:19], v[18:19], v[20:21]
	v_rcp_f32_e32 v16, v16
	v_rcp_f32_e32 v17, v17
	v_rcp_f32_e32 v18, v18
	v_rcp_f32_e32 v19, v19
	v_pk_mul_f32 v[106:107], v[106:107], v[206:207] op_sel:[0,1] op_sel_hi:[1,1]
	v_pk_mul_f32 v[108:109], v[108:109], v[206:207] op_sel:[0,1] op_sel_hi:[1,1]
	v_pk_mul_f32 v[102:103], v[102:103], v[16:17]
	v_pk_mul_f32 v[104:105], v[104:105], v[18:19]
	v_pk_mul_f32 v[102:103], v[102:103], v[106:107]
	v_pk_mul_f32 v[104:105], v[104:105], v[108:109]
	v_med3_f32 v102, v102, s35, v225
	v_med3_f32 v103, v103, s35, v225
	v_med3_f32 v104, v104, s35, v225
	v_med3_f32 v105, v105, s35, v225
	v_cvt_pk_fp8_f32 v126, v126, v127
	v_cvt_pk_fp8_f32 v127, v118, v119
	v_cvt_pk_fp8_f32 v126, v128, v129 op_sel:[0,0,1]
	v_cvt_pk_fp8_f32 v127, v120, v121 op_sel:[0,0,1]
	v_cvt_pk_fp8_f32 v128, v110, v111
	v_cvt_pk_fp8_f32 v129, v102, v103
	v_cvt_pk_fp8_f32 v128, v112, v113 op_sel:[0,0,1]
	v_cvt_pk_fp8_f32 v129, v104, v105 op_sel:[0,0,1]
	v_add_co_u32_e32 v12, vcc, 0x20000, v10
	s_nop 0
	v_permlane16_swap_b32_e32 v126, v128
	v_addc_co_u32_e32 v13, vcc, 0, v11, vcc
	v_permlane16_swap_b32_e32 v127, v129
	global_store_dwordx4 v[12:13], v[126:129], off
	v_mul_f32_e32 v16, 0xbcb8aa3b, v94
	v_mul_f32_e32 v17, 0xbcb8aa3b, v95
	v_mul_f32_e32 v18, 0xbcb8aa3b, v96
	v_mul_f32_e32 v19, 0xbcb8aa3b, v97
	v_exp_f32_e32 v16, v16
	v_exp_f32_e32 v17, v17
	v_exp_f32_e32 v18, v18
	v_exp_f32_e32 v19, v19
	v_pk_add_f32 v[16:17], v[16:17], v[20:21]
	v_pk_add_f32 v[18:19], v[18:19], v[20:21]
	v_rcp_f32_e32 v16, v16
	v_rcp_f32_e32 v17, v17
	v_rcp_f32_e32 v18, v18
	v_rcp_f32_e32 v19, v19
	v_pk_mul_f32 v[98:99], v[98:99], v[206:207] op_sel:[0,1] op_sel_hi:[1,1]
	v_pk_mul_f32 v[100:101], v[100:101], v[206:207] op_sel:[0,1] op_sel_hi:[1,1]
	v_pk_mul_f32 v[94:95], v[94:95], v[16:17]
	v_pk_mul_f32 v[96:97], v[96:97], v[18:19]
	v_pk_mul_f32 v[94:95], v[94:95], v[98:99]
	v_pk_mul_f32 v[96:97], v[96:97], v[100:101]
	v_med3_f32 v94, v94, s35, v225
	v_med3_f32 v95, v95, s35, v225
	v_med3_f32 v96, v96, s35, v225
	v_med3_f32 v97, v97, s35, v225
	v_mul_f32_e32 v16, 0xbcb8aa3b, v86
	v_mul_f32_e32 v17, 0xbcb8aa3b, v87
	v_mul_f32_e32 v18, 0xbcb8aa3b, v88
	v_mul_f32_e32 v19, 0xbcb8aa3b, v89
	v_exp_f32_e32 v16, v16
	v_exp_f32_e32 v17, v17
	v_exp_f32_e32 v18, v18
	v_exp_f32_e32 v19, v19
	v_pk_add_f32 v[16:17], v[16:17], v[20:21]
	v_pk_add_f32 v[18:19], v[18:19], v[20:21]
	v_rcp_f32_e32 v16, v16
	v_rcp_f32_e32 v17, v17
	v_rcp_f32_e32 v18, v18
	v_rcp_f32_e32 v19, v19
	v_pk_mul_f32 v[90:91], v[90:91], v[206:207] op_sel:[0,1] op_sel_hi:[1,1]
	v_pk_mul_f32 v[92:93], v[92:93], v[206:207] op_sel:[0,1] op_sel_hi:[1,1]
	v_pk_mul_f32 v[86:87], v[86:87], v[16:17]
	v_pk_mul_f32 v[88:89], v[88:89], v[18:19]
	v_pk_mul_f32 v[86:87], v[86:87], v[90:91]
	v_pk_mul_f32 v[88:89], v[88:89], v[92:93]
	v_med3_f32 v86, v86, s35, v225
	v_med3_f32 v87, v87, s35, v225
	v_med3_f32 v88, v88, s35, v225
	v_med3_f32 v89, v89, s35, v225
	v_mul_f32_e32 v16, 0xbcb8aa3b, v78
	v_mul_f32_e32 v17, 0xbcb8aa3b, v79
	v_mul_f32_e32 v18, 0xbcb8aa3b, v80
	v_mul_f32_e32 v19, 0xbcb8aa3b, v81
	v_exp_f32_e32 v16, v16
	v_exp_f32_e32 v17, v17
	v_exp_f32_e32 v18, v18
	v_exp_f32_e32 v19, v19
	v_pk_add_f32 v[16:17], v[16:17], v[20:21]
	v_pk_add_f32 v[18:19], v[18:19], v[20:21]
	v_rcp_f32_e32 v16, v16
	v_rcp_f32_e32 v17, v17
	v_rcp_f32_e32 v18, v18
	v_rcp_f32_e32 v19, v19
	v_pk_mul_f32 v[82:83], v[82:83], v[206:207] op_sel:[0,1] op_sel_hi:[1,1]
	v_pk_mul_f32 v[84:85], v[84:85], v[206:207] op_sel:[0,1] op_sel_hi:[1,1]
	v_pk_mul_f32 v[78:79], v[78:79], v[16:17]
	v_pk_mul_f32 v[80:81], v[80:81], v[18:19]
	v_pk_mul_f32 v[78:79], v[78:79], v[82:83]
	v_pk_mul_f32 v[80:81], v[80:81], v[84:85]
	v_med3_f32 v78, v78, s35, v225
	v_med3_f32 v79, v79, s35, v225
	v_med3_f32 v80, v80, s35, v225
	v_med3_f32 v81, v81, s35, v225
	v_mul_f32_e32 v16, 0xbcb8aa3b, v70
	v_mul_f32_e32 v17, 0xbcb8aa3b, v71
	v_mul_f32_e32 v18, 0xbcb8aa3b, v72
	v_mul_f32_e32 v19, 0xbcb8aa3b, v73
	v_exp_f32_e32 v16, v16
	v_exp_f32_e32 v17, v17
	v_exp_f32_e32 v18, v18
	v_exp_f32_e32 v19, v19
	v_pk_add_f32 v[16:17], v[16:17], v[20:21]
	v_pk_add_f32 v[18:19], v[18:19], v[20:21]
	v_rcp_f32_e32 v16, v16
	v_rcp_f32_e32 v17, v17
	v_rcp_f32_e32 v18, v18
	v_rcp_f32_e32 v19, v19
	v_pk_mul_f32 v[74:75], v[74:75], v[206:207] op_sel:[0,1] op_sel_hi:[1,1]
	v_pk_mul_f32 v[76:77], v[76:77], v[206:207] op_sel:[0,1] op_sel_hi:[1,1]
	v_pk_mul_f32 v[70:71], v[70:71], v[16:17]
	v_pk_mul_f32 v[72:73], v[72:73], v[18:19]
	v_pk_mul_f32 v[70:71], v[70:71], v[74:75]
	v_pk_mul_f32 v[72:73], v[72:73], v[76:77]
	v_med3_f32 v70, v70, s35, v225
	v_med3_f32 v71, v71, s35, v225
	v_med3_f32 v72, v72, s35, v225
	v_med3_f32 v73, v73, s35, v225
	v_cvt_pk_fp8_f32 v94, v94, v95
	v_cvt_pk_fp8_f32 v95, v86, v87
	v_cvt_pk_fp8_f32 v94, v96, v97 op_sel:[0,0,1]
	v_cvt_pk_fp8_f32 v95, v88, v89 op_sel:[0,0,1]
	v_cvt_pk_fp8_f32 v96, v78, v79
	v_cvt_pk_fp8_f32 v97, v70, v71
	v_cvt_pk_fp8_f32 v96, v80, v81 op_sel:[0,0,1]
	v_cvt_pk_fp8_f32 v97, v72, v73 op_sel:[0,0,1]
	v_add_co_u32_e32 v12, vcc, 0x28000, v10
	s_nop 0
	v_permlane16_swap_b32_e32 v94, v96
	v_addc_co_u32_e32 v13, vcc, 0, v11, vcc
	v_permlane16_swap_b32_e32 v95, v97
	global_store_dwordx4 v[12:13], v[94:97], off
	s_and_b64 vcc, exec, s[40:41]
	s_cbranch_vccnz .LBB0_1356
	v_readlane_b32 s6, v255, 14
	v_readlane_b32 s7, v255, 15
	s_andn2_b64 vcc, exec, s[6:7]
	s_cbranch_vccnz .LBB0_1355
	s_barrier
	s_branch .LBB0_1355

; #define GAS __attribute__((address_space(1)))
; DI int rfl(int v) { return __builtin_amdgcn_readfirstlane(v); }
;     DI void operator()(const f32x4 (&acc)[2][2][4][2], const Unit& u, int wr, int wc, int fr, int fq) const {
;         asm volatile("" : "+v"(fr), "+v"(fq));
;         const int lrow0 = wr * 64 + fr, col0 = u.pn * 256 + wc * 32 + 8 * fq; const int lt = u.pm - rfl(pre[u.e]);
;         const int* lp = list + (size_t)u.e * T + 256 * lt;
;         int slotv[8];
; #pragma unroll
;         for (int q = 0; q < 8; ++q) { const int r = lrow0 + (q >> 2) * 128 + (q & 3) * 16; slotv[q] = ((const GAS int*)lp)[r < u.nv ? r : 0]; }
.LBB0_1644:
	s_mov_b64 s[98:99], s[46:47]
	v_mov_b32_e32 v11, v5
	v_mov_b32_e32 v6, v1
	v_readlane_b32 s6, v254, 36
	s_nop 15
	s_ashr_i32 s45, s44, 31
	v_readlane_b32 s9, v254, 38
	v_add_u32_e32 v24, s6, v6
	s_lshl_b32 s6, s44, 2
	s_add_i32 s6, s39, s6
	v_mov_b32_e32 v6, s6
	ds_read_b32 v6, v6
	v_cmp_gt_i32_e64 s[54:55], s93, v24
	s_waitcnt lgkmcnt(0)
	v_readfirstlane_b32 s6, v6
	s_sub_i32 s8, s42, s6
	s_lshl_b64 s[6:7], s[44:45], 18
	s_add_u32 s9, s9, s6
	v_readlane_b32 s6, v254, 34
	s_addc_u32 s10, s6, s7
	s_lshl_b32 s6, s8, 8
	s_ashr_i32 s7, s6, 31
	v_add_u32_e32 v6, 16, v24
	s_lshl_b64 s[6:7], s[6:7], 2
	v_cmp_gt_i32_e64 s[52:53], s93, v6
	s_add_u32 s30, s9, s6
	s_addc_u32 s31, s10, s7
	v_cndmask_b32_e64 v6, 0, v6, s[52:53]
	v_ashrrev_i32_e32 v7, 31, v6
	v_lshl_add_u64 v[6:7], v[6:7], 2, s[30:31]
	v_mov_b32_e32 v22, v206
	v_add_u32_e32 v6, 32, v24
	v_cmp_gt_i32_e64 s[50:51], s93, v6
	s_lshl_b32 s6, s66, 8
	s_or_b32 s6, s6, s95
	v_cndmask_b32_e64 v6, 0, v6, s[50:51]
	v_ashrrev_i32_e32 v7, 31, v6
	v_lshl_add_u64 v[6:7], v[6:7], 2, s[30:31]
	v_mov_b32_e32 v20, v235
	v_add_u32_e32 v6, 48, v24
	v_cmp_gt_i32_e64 s[48:49], s93, v6
	v_lshl_add_u32 v8, v11, 3, s6
	v_ashrrev_i32_e32 v9, 31, v8
	v_cndmask_b32_e64 v6, 0, v6, s[48:49]
	v_ashrrev_i32_e32 v7, 31, v6
	v_lshl_add_u64 v[6:7], v[6:7], 2, s[30:31]
	v_mov_b32_e32 v18, v244
	v_add_u32_e32 v6, 0x80, v24
	v_cmp_gt_i32_e64 s[46:47], s93, v6
	s_nop 1
	v_cndmask_b32_e64 v6, 0, v6, s[46:47]
	v_ashrrev_i32_e32 v7, 31, v6
	v_lshl_add_u64 v[6:7], v[6:7], 2, s[30:31]
	v_mov_b32_e32 v16, v245
	v_add_u32_e32 v6, 0x90, v24
	v_cmp_gt_i32_e64 s[44:45], s93, v6
	s_nop 1
	v_cndmask_b32_e64 v6, 0, v6, s[44:45]
	v_ashrrev_i32_e32 v7, 31, v6
	v_lshl_add_u64 v[6:7], v[6:7], 2, s[30:31]
	v_mov_b32_e32 v14, v246
	v_add_u32_e32 v6, 0xa0, v24
	v_cmp_gt_i32_e64 s[42:43], s93, v6
	s_nop 1
	v_cndmask_b32_e64 v6, 0, v6, s[42:43]
	v_ashrrev_i32_e32 v7, 31, v6
	v_lshl_add_u64 v[6:7], v[6:7], 2, s[30:31]
	v_mov_b32_e32 v12, v247
	v_add_u32_e32 v6, 0xb0, v24
	v_cmp_gt_i32_e32 vcc, s93, v6
	s_nop 1
	v_cndmask_b32_e32 v6, 0, v6, vcc
	v_ashrrev_i32_e32 v7, 31, v6
	v_lshl_add_u64 v[6:7], v[6:7], 2, s[30:31]
	v_mov_b32_e32 v10, v249
	v_bfe_i32 v6, v11, 0, 1
	v_and_b32_e32 v6, 0x78, v6
	v_mov_b32_e32 v7, v4
	v_mov_b32_e32 v25, v203
	s_cmp_eq_u64 s[98:99], 0
	s_cbranch_scc1 .Lm2_noslot
	s_lshl_b32 s98, s60, 2
	s_add_i32 s98, s39, s98
	v_mov_b32_e32 v203, s98
	ds_read_b32 v203, v203
	v_readlane_b32 s100, v254, 38
	v_readlane_b32 s101, v254, 34
	s_lshl_b32 s98, s60, 18
	s_add_u32 s100, s100, s98
	s_addc_u32 s101, s101, 0
	s_waitcnt lgkmcnt(0)
	v_readfirstlane_b32 s98, v203
	s_sub_i32 s98, s16, s98
	s_lshl_b32 s98, s98, 10
	s_ashr_i32 s99, s98, 31
	s_add_u32 s100, s100, s98
	s_addc_u32 s101, s101, s99
	v_readlane_b32 s98, v254, 36
	s_nop 1
	v_add_u32_e32 v203, s98, v1
	v_add_u32_e32 v206, 0x10, v203
	v_add_u32_e32 v235, 0x20, v203
	v_add_u32_e32 v244, 0x30, v203
	v_add_u32_e32 v245, 0x80, v203
	v_add_u32_e32 v246, 0x90, v203
	v_add_u32_e32 v247, 0xa0, v203
	v_add_u32_e32 v249, 0xb0, v203
	v_cmp_gt_i32_e64 s[98:99], s94, v206
	s_nop 1
	v_cndmask_b32_e64 v206, 0, v206, s[98:99]
	v_lshlrev_b32_e32 v206, 2, v206
	global_load_dword v206, v206, s[100:101]
	v_cmp_gt_i32_e64 s[98:99], s94, v235
	s_nop 1
	v_cndmask_b32_e64 v235, 0, v235, s[98:99]
	v_lshlrev_b32_e32 v235, 2, v235
	global_load_dword v235, v235, s[100:101]
	v_cmp_gt_i32_e64 s[98:99], s94, v244
	s_nop 1
	v_cndmask_b32_e64 v244, 0, v244, s[98:99]
	v_lshlrev_b32_e32 v244, 2, v244
	global_load_dword v244, v244, s[100:101]
	v_cmp_gt_i32_e64 s[98:99], s94, v245
	s_nop 1
	v_cndmask_b32_e64 v245, 0, v245, s[98:99]
	v_lshlrev_b32_e32 v245, 2, v245
	global_load_dword v245, v245, s[100:101]
	v_cmp_gt_i32_e64 s[98:99], s94, v246
	s_nop 1
	v_cndmask_b32_e64 v246, 0, v246, s[98:99]
	v_lshlrev_b32_e32 v246, 2, v246
	global_load_dword v246, v246, s[100:101]
	v_cmp_gt_i32_e64 s[98:99], s94, v247
	s_nop 1
	v_cndmask_b32_e64 v247, 0, v247, s[98:99]
	v_lshlrev_b32_e32 v247, 2, v247
	global_load_dword v247, v247, s[100:101]
	v_cmp_gt_i32_e64 s[98:99], s94, v249
	s_nop 1
	v_cndmask_b32_e64 v249, 0, v249, s[98:99]
	v_lshlrev_b32_e32 v249, 2, v249
	global_load_dword v249, v249, s[100:101]
	v_cmp_gt_i32_e64 s[98:99], s94, v203
	s_nop 1
	v_cndmask_b32_e64 v203, 0, v203, s[98:99]
	v_lshlrev_b32_e32 v203, 2, v203
	global_load_dword v203, v203, s[100:101]
